# E2 expert output item loop rewritten by hand like E1: double-buffered gathers, x and g2 rows prefetched one token ahead, reduce in dead gather registers
# speedup vs baseline: 1.0235x; 1.0070x over previous
.LBB0_886:
	s_or_b64 exec, exec, s[0:1]
	v_mov_b32_e32 v2, s92
	s_waitcnt lgkmcnt(0)
	s_barrier
	ds_read_b32 v2, v2
	s_mov_b64 s[0:1], -1
	s_waitcnt lgkmcnt(0)
	v_readfirstlane_b32 s2, v2
	s_cmp_ge_i32 s2, s60
	s_cbranch_scc1 .LBB0_881
	s_and_b32 s0, s2, 0xffffff00
	s_lshl_b32 s3, s2, 6
	s_add_i32 s2, s0, 0x100
	s_and_b64 s[0:1], s[30:31], exec
	s_cselect_b32 s0, 0, s2
	s_add_i32 s0, s0, s3
	v_and_b32_e32 v242, 7, v0
	v_lshrrev_b32_e32 v243, 6, v0
	v_bfe_u32 v244, v0, 3, 3
	v_bfe_u32 v245, v0, 3, 1
	v_lshl_add_u32 v226, v243, 3, s0
	v_lshlrev_b32_e32 v218, 4, v242
	v_lshlrev_b32_e32 v219, 8, v226
	v_lshl_add_u32 v219, v244, 5, v219
	v_lshl_or_b32 v246, v242, 5, s58
	v_lshrrev_b32_e32 v247, 1, v0
	v_and_b32_e32 v247, 24, v247
	v_lshlrev_b32_e32 v248, 2, v245
	v_or3_b32 v246, v246, v247, v248
	v_lshlrev_b32_e32 v236, 2, v246
	v_mov_b32_e32 v237, 0
	v_cmp_eq_u32_e64 s[38:39], 0, v245
	global_load_dwordx4 v[162:165], v219, s[22:23]
	global_load_dwordx4 v[166:169], v219, s[22:23] offset:16
	global_load_dwordx4 v[170:173], v219, s[22:23] offset:256
	global_load_dwordx4 v[174:177], v219, s[22:23] offset:272
	s_waitcnt vmcnt(2)
	v_and_b32_e32 v194, 0xffff, v162
	v_lshrrev_b32_e32 v195, 16, v162
	v_lshl_add_u32 v194, v194, 7, v218
	v_lshl_add_u32 v195, v195, 7, v218
	global_load_dwordx4 v[2:5], v194, s[40:41]
	global_load_dwordx4 v[6:9], v195, s[40:41]
	v_and_b32_e32 v194, 0xffff, v163
	v_lshrrev_b32_e32 v195, 16, v163
	v_lshl_add_u32 v194, v194, 7, v218
	v_lshl_add_u32 v195, v195, 7, v218
	global_load_dwordx4 v[10:13], v194, s[40:41]
	global_load_dwordx4 v[14:17], v195, s[40:41]
	v_and_b32_e32 v194, 0xffff, v164
	v_lshrrev_b32_e32 v195, 16, v164
	v_lshl_add_u32 v194, v194, 7, v218
	v_lshl_add_u32 v195, v195, 7, v218
	global_load_dwordx4 v[18:21], v194, s[40:41]
	global_load_dwordx4 v[22:25], v195, s[40:41]
	v_and_b32_e32 v194, 0xffff, v165
	v_lshrrev_b32_e32 v195, 16, v165
	v_lshl_add_u32 v194, v194, 7, v218
	v_lshl_add_u32 v195, v195, 7, v218
	global_load_dwordx4 v[26:29], v194, s[40:41]
	global_load_dwordx4 v[30:33], v195, s[40:41]
	v_and_b32_e32 v194, 0xffff, v166
	v_lshrrev_b32_e32 v195, 16, v166
	v_lshl_add_u32 v194, v194, 7, v218
	v_lshl_add_u32 v195, v195, 7, v218
	global_load_dwordx4 v[34:37], v194, s[40:41]
	global_load_dwordx4 v[38:41], v195, s[40:41]
	v_and_b32_e32 v194, 0xffff, v167
	v_lshrrev_b32_e32 v195, 16, v167
	v_lshl_add_u32 v194, v194, 7, v218
	v_lshl_add_u32 v195, v195, 7, v218
	global_load_dwordx4 v[42:45], v194, s[40:41]
	global_load_dwordx4 v[46:49], v195, s[40:41]
	v_and_b32_e32 v194, 0xffff, v168
	v_lshrrev_b32_e32 v195, 16, v168
	v_lshl_add_u32 v194, v194, 7, v218
	v_lshl_add_u32 v195, v195, 7, v218
	global_load_dwordx4 v[50:53], v194, s[40:41]
	global_load_dwordx4 v[54:57], v195, s[40:41]
	v_and_b32_e32 v194, 0xffff, v169
	v_lshrrev_b32_e32 v195, 16, v169
	v_lshl_add_u32 v194, v194, 7, v218
	v_lshl_add_u32 v195, v195, 7, v218
	global_load_dwordx4 v[58:61], v194, s[40:41]
	global_load_dwordx4 v[62:65], v195, s[40:41]
	global_load_dwordx4 v[130:133], v219, s[56:57] offset:-272
	global_load_dwordx4 v[134:137], v219, s[56:57] offset:-256
	v_add_u32_e32 v250, 0, v226
	v_mul_hi_i32 v242, v250, s69
	v_lshrrev_b32_e32 v243, 31, v242
	v_ashrrev_i32_e32 v242, 13, v242
	v_add_u32_e32 v243, v242, v243
	v_mul_i32_i24_e32 v246, 0xffffbf00, v243
	v_add_u32_e32 v242, v250, v246
	v_cmp_gt_i32_e32 vcc, s68, v242
	v_cmp_lt_i32_e64 s[0:1], s21, v242
	s_and_saveexec_b64 s[2:3], s[0:1]
	s_xor_b64 s[0:1], exec, s[2:3]
	v_lshl_add_u32 v242, v243, 14, v246
	v_add3_u32 v242, v250, v242, s88
	s_or_saveexec_b64 s[0:1], s[0:1]
	v_mov_b64_e32 v[244:245], s[18:19]
	s_xor_b64 exec, exec, s[0:1]
	v_lshlrev_b32_e32 v242, 8, v243
	v_add3_u32 v242, v246, v250, v242
	v_mov_b64_e32 v[244:245], s[72:73]
	s_or_b64 exec, exec, s[0:1]
	v_mul_i32_i24_e32 v243, 0x3000, v243
	v_cndmask_b32_e32 v246, v243, v223, vcc
	v_ashrrev_i32_e32 v247, 31, v246
	v_lshl_add_u64 v[246:247], v[246:247], 2, s[10:11]
	v_ashrrev_i32_e32 v243, 31, v242
	v_lshl_add_u64 v[248:249], v[246:247], 0, v[236:237]
	v_lshlrev_b64 v[242:243], 13, v[242:243]
	v_lshl_add_u64 v[242:243], v[244:245], 0, v[242:243]
	v_add_co_u32_e32 v248, vcc, s94, v248
	v_lshl_add_u64 v[238:239], v[242:243], 0, v[236:237]
	s_nop 0
	v_addc_co_u32_e32 v249, vcc, 0, v249, vcc
	global_load_dwordx4 v[146:149], v[238:239], off
	global_load_dwordx4 v[150:153], v[248:249], off
	v_add_u32_e32 v219, 0x200, v219
	s_mov_b32 s33, 0
	s_waitcnt vmcnt(0)
.Le2_loop:
	s_waitcnt vmcnt(1)
	v_and_b32_e32 v194, 0xffff, v170
	v_lshrrev_b32_e32 v195, 16, v170
	v_lshl_add_u32 v194, v194, 7, v218
	v_lshl_add_u32 v195, v195, 7, v218
	global_load_dwordx4 v[66:69], v194, s[40:41]
	global_load_dwordx4 v[70:73], v195, s[40:41]
	v_and_b32_e32 v194, 0xffff, v171
	v_lshrrev_b32_e32 v195, 16, v171
	v_lshl_add_u32 v194, v194, 7, v218
	v_lshl_add_u32 v195, v195, 7, v218
	global_load_dwordx4 v[74:77], v194, s[40:41]
	global_load_dwordx4 v[78:81], v195, s[40:41]
	v_and_b32_e32 v194, 0xffff, v172
	v_lshrrev_b32_e32 v195, 16, v172
	v_lshl_add_u32 v194, v194, 7, v218
	v_lshl_add_u32 v195, v195, 7, v218
	global_load_dwordx4 v[82:85], v194, s[40:41]
	global_load_dwordx4 v[86:89], v195, s[40:41]
	v_and_b32_e32 v194, 0xffff, v173
	v_lshrrev_b32_e32 v195, 16, v173
	v_lshl_add_u32 v194, v194, 7, v218
	v_lshl_add_u32 v195, v195, 7, v218
	global_load_dwordx4 v[90:93], v194, s[40:41]
	global_load_dwordx4 v[94:97], v195, s[40:41]
	v_and_b32_e32 v194, 0xffff, v174
	v_lshrrev_b32_e32 v195, 16, v174
	v_lshl_add_u32 v194, v194, 7, v218
	v_lshl_add_u32 v195, v195, 7, v218
	global_load_dwordx4 v[98:101], v194, s[40:41]
	global_load_dwordx4 v[102:105], v195, s[40:41]
	v_and_b32_e32 v194, 0xffff, v175
	v_lshrrev_b32_e32 v195, 16, v175
	v_lshl_add_u32 v194, v194, 7, v218
	v_lshl_add_u32 v195, v195, 7, v218
	global_load_dwordx4 v[106:109], v194, s[40:41]
	global_load_dwordx4 v[110:113], v195, s[40:41]
	v_and_b32_e32 v194, 0xffff, v176
	v_lshrrev_b32_e32 v195, 16, v176
	v_lshl_add_u32 v194, v194, 7, v218
	v_lshl_add_u32 v195, v195, 7, v218
	global_load_dwordx4 v[114:117], v194, s[40:41]
	global_load_dwordx4 v[118:121], v195, s[40:41]
	v_and_b32_e32 v194, 0xffff, v177
	v_lshrrev_b32_e32 v195, 16, v177
	v_lshl_add_u32 v194, v194, 7, v218
	v_lshl_add_u32 v195, v195, 7, v218
	global_load_dwordx4 v[122:125], v194, s[40:41]
	global_load_dwordx4 v[126:129], v195, s[40:41]
	global_load_dwordx4 v[138:141], v219, s[56:57] offset:-528
	global_load_dwordx4 v[142:145], v219, s[56:57] offset:-512
	v_add_u32_e32 v250, 1, v226
	v_mul_hi_i32 v242, v250, s69
	v_lshrrev_b32_e32 v243, 31, v242
	v_ashrrev_i32_e32 v242, 13, v242
	v_add_u32_e32 v243, v242, v243
	v_mul_i32_i24_e32 v246, 0xffffbf00, v243
	v_add_u32_e32 v242, v250, v246
	v_cmp_gt_i32_e32 vcc, s68, v242
	v_cmp_lt_i32_e64 s[0:1], s21, v242
	s_and_saveexec_b64 s[2:3], s[0:1]
	s_xor_b64 s[0:1], exec, s[2:3]
	v_lshl_add_u32 v242, v243, 14, v246
	v_add3_u32 v242, v250, v242, s88
	s_or_saveexec_b64 s[0:1], s[0:1]
	v_mov_b64_e32 v[244:245], s[18:19]
	s_xor_b64 exec, exec, s[0:1]
	v_lshlrev_b32_e32 v242, 8, v243
	v_add3_u32 v242, v246, v250, v242
	v_mov_b64_e32 v[244:245], s[72:73]
	s_or_b64 exec, exec, s[0:1]
	v_mul_i32_i24_e32 v243, 0x3000, v243
	v_cndmask_b32_e32 v246, v243, v223, vcc
	v_ashrrev_i32_e32 v247, 31, v246
	v_lshl_add_u64 v[246:247], v[246:247], 2, s[10:11]
	v_ashrrev_i32_e32 v243, 31, v242
	v_lshl_add_u64 v[248:249], v[246:247], 0, v[236:237]
	v_lshlrev_b64 v[242:243], 13, v[242:243]
	v_lshl_add_u64 v[242:243], v[244:245], 0, v[242:243]
	v_add_co_u32_e32 v248, vcc, s94, v248
	v_lshl_add_u64 v[240:241], v[242:243], 0, v[236:237]
	s_nop 0
	v_addc_co_u32_e32 v249, vcc, 0, v249, vcc
	global_load_dwordx4 v[154:157], v[240:241], off
	global_load_dwordx4 v[158:161], v[248:249], off
	s_cmp_lt_u32 s33, 6
	s_cbranch_scc0 .Le2_skipA
	global_load_dwordx4 v[162:165], v219, s[22:23]
	global_load_dwordx4 v[166:169], v219, s[22:23] offset:16
.Le2_skipA:
	v_mul_u32_u24_sdwa v202, v130, s93 dst_sel:DWORD dst_unused:UNUSED_PAD src0_sel:WORD_0 src1_sel:DWORD
	v_cvt_scalef32_pk_f16_fp4 v194, v2, 1.0
	v_cvt_scalef32_pk_f16_fp4 v195, v2, 1.0 op_sel:[1,0,0]
	v_cvt_scalef32_pk_f16_fp4 v196, v2, 1.0 op_sel:[0,1,0]
	v_pk_fma_f16 v178, v194, v202, 0
	v_cvt_scalef32_pk_f16_fp4 v197, v2, 1.0 op_sel:[1,1,0]
	v_pk_fma_f16 v179, v195, v202, 0
	v_cvt_scalef32_pk_f16_fp4 v194, v3, 1.0
	v_pk_fma_f16 v180, v196, v202, 0
	v_cvt_scalef32_pk_f16_fp4 v195, v3, 1.0 op_sel:[1,0,0]
	v_pk_fma_f16 v181, v197, v202, 0
	v_cvt_scalef32_pk_f16_fp4 v196, v3, 1.0 op_sel:[0,1,0]
	v_pk_fma_f16 v182, v194, v202, 0
	v_cvt_scalef32_pk_f16_fp4 v197, v3, 1.0 op_sel:[1,1,0]
	v_pk_fma_f16 v183, v195, v202, 0
	v_cvt_scalef32_pk_f16_fp4 v194, v4, 1.0
	v_pk_fma_f16 v184, v196, v202, 0
	v_cvt_scalef32_pk_f16_fp4 v195, v4, 1.0 op_sel:[1,0,0]
	v_pk_fma_f16 v185, v197, v202, 0
	v_cvt_scalef32_pk_f16_fp4 v196, v4, 1.0 op_sel:[0,1,0]
	v_pk_fma_f16 v186, v194, v202, 0
	v_cvt_scalef32_pk_f16_fp4 v197, v4, 1.0 op_sel:[1,1,0]
	v_pk_fma_f16 v187, v195, v202, 0
	v_cvt_scalef32_pk_f16_fp4 v194, v5, 1.0
	v_pk_fma_f16 v188, v196, v202, 0
	v_cvt_scalef32_pk_f16_fp4 v195, v5, 1.0 op_sel:[1,0,0]
	v_pk_fma_f16 v189, v197, v202, 0
	v_cvt_scalef32_pk_f16_fp4 v196, v5, 1.0 op_sel:[0,1,0]
	v_pk_fma_f16 v190, v194, v202, 0
	v_cvt_scalef32_pk_f16_fp4 v197, v5, 1.0 op_sel:[1,1,0]
	v_pk_fma_f16 v191, v195, v202, 0
	v_pk_fma_f16 v192, v196, v202, 0
	v_pk_fma_f16 v193, v197, v202, 0
	v_mul_u32_u24_sdwa v203, v130, s93 dst_sel:DWORD dst_unused:UNUSED_PAD src0_sel:WORD_1 src1_sel:DWORD
	v_cvt_scalef32_pk_f16_fp4 v194, v6, 1.0
	v_cvt_scalef32_pk_f16_fp4 v195, v6, 1.0 op_sel:[1,0,0]
	v_cvt_scalef32_pk_f16_fp4 v196, v6, 1.0 op_sel:[0,1,0]
	v_pk_fma_f16 v178, v194, v203, v178
	v_cvt_scalef32_pk_f16_fp4 v197, v6, 1.0 op_sel:[1,1,0]
	v_pk_fma_f16 v179, v195, v203, v179
	v_cvt_scalef32_pk_f16_fp4 v194, v7, 1.0
	v_pk_fma_f16 v180, v196, v203, v180
	v_cvt_scalef32_pk_f16_fp4 v195, v7, 1.0 op_sel:[1,0,0]
	v_pk_fma_f16 v181, v197, v203, v181
	v_cvt_scalef32_pk_f16_fp4 v196, v7, 1.0 op_sel:[0,1,0]
	v_pk_fma_f16 v182, v194, v203, v182
	v_cvt_scalef32_pk_f16_fp4 v197, v7, 1.0 op_sel:[1,1,0]
	v_pk_fma_f16 v183, v195, v203, v183
	v_cvt_scalef32_pk_f16_fp4 v194, v8, 1.0
	v_pk_fma_f16 v184, v196, v203, v184
	v_cvt_scalef32_pk_f16_fp4 v195, v8, 1.0 op_sel:[1,0,0]
	v_pk_fma_f16 v185, v197, v203, v185
	v_cvt_scalef32_pk_f16_fp4 v196, v8, 1.0 op_sel:[0,1,0]
	v_pk_fma_f16 v186, v194, v203, v186
	v_cvt_scalef32_pk_f16_fp4 v197, v8, 1.0 op_sel:[1,1,0]
	v_pk_fma_f16 v187, v195, v203, v187
	v_cvt_scalef32_pk_f16_fp4 v194, v9, 1.0
	v_pk_fma_f16 v188, v196, v203, v188
	v_cvt_scalef32_pk_f16_fp4 v195, v9, 1.0 op_sel:[1,0,0]
	v_pk_fma_f16 v189, v197, v203, v189
	v_cvt_scalef32_pk_f16_fp4 v196, v9, 1.0 op_sel:[0,1,0]
	v_pk_fma_f16 v190, v194, v203, v190
	v_cvt_scalef32_pk_f16_fp4 v197, v9, 1.0 op_sel:[1,1,0]
	v_pk_fma_f16 v191, v195, v203, v191
	v_pk_fma_f16 v192, v196, v203, v192
	v_pk_fma_f16 v193, v197, v203, v193
	v_mul_u32_u24_sdwa v202, v131, s93 dst_sel:DWORD dst_unused:UNUSED_PAD src0_sel:WORD_0 src1_sel:DWORD
	v_cvt_scalef32_pk_f16_fp4 v194, v10, 1.0
	v_cvt_scalef32_pk_f16_fp4 v195, v10, 1.0 op_sel:[1,0,0]
	v_cvt_scalef32_pk_f16_fp4 v196, v10, 1.0 op_sel:[0,1,0]
	v_pk_fma_f16 v178, v194, v202, v178
	v_cvt_scalef32_pk_f16_fp4 v197, v10, 1.0 op_sel:[1,1,0]
	v_pk_fma_f16 v179, v195, v202, v179
	v_cvt_scalef32_pk_f16_fp4 v194, v11, 1.0
	v_pk_fma_f16 v180, v196, v202, v180
	v_cvt_scalef32_pk_f16_fp4 v195, v11, 1.0 op_sel:[1,0,0]
	v_pk_fma_f16 v181, v197, v202, v181
	v_cvt_scalef32_pk_f16_fp4 v196, v11, 1.0 op_sel:[0,1,0]
	v_pk_fma_f16 v182, v194, v202, v182
	v_cvt_scalef32_pk_f16_fp4 v197, v11, 1.0 op_sel:[1,1,0]
	v_pk_fma_f16 v183, v195, v202, v183
	v_cvt_scalef32_pk_f16_fp4 v194, v12, 1.0
	v_pk_fma_f16 v184, v196, v202, v184
	v_cvt_scalef32_pk_f16_fp4 v195, v12, 1.0 op_sel:[1,0,0]
	v_pk_fma_f16 v185, v197, v202, v185
	v_cvt_scalef32_pk_f16_fp4 v196, v12, 1.0 op_sel:[0,1,0]
	v_pk_fma_f16 v186, v194, v202, v186
	v_cvt_scalef32_pk_f16_fp4 v197, v12, 1.0 op_sel:[1,1,0]
	v_pk_fma_f16 v187, v195, v202, v187
	v_cvt_scalef32_pk_f16_fp4 v194, v13, 1.0
	v_pk_fma_f16 v188, v196, v202, v188
	v_cvt_scalef32_pk_f16_fp4 v195, v13, 1.0 op_sel:[1,0,0]
	v_pk_fma_f16 v189, v197, v202, v189
	v_cvt_scalef32_pk_f16_fp4 v196, v13, 1.0 op_sel:[0,1,0]
	v_pk_fma_f16 v190, v194, v202, v190
	v_cvt_scalef32_pk_f16_fp4 v197, v13, 1.0 op_sel:[1,1,0]
	v_pk_fma_f16 v191, v195, v202, v191
	v_pk_fma_f16 v192, v196, v202, v192
	v_pk_fma_f16 v193, v197, v202, v193
	v_mul_u32_u24_sdwa v203, v131, s93 dst_sel:DWORD dst_unused:UNUSED_PAD src0_sel:WORD_1 src1_sel:DWORD
	v_cvt_scalef32_pk_f16_fp4 v194, v14, 1.0
	v_cvt_scalef32_pk_f16_fp4 v195, v14, 1.0 op_sel:[1,0,0]
	v_cvt_scalef32_pk_f16_fp4 v196, v14, 1.0 op_sel:[0,1,0]
	v_pk_fma_f16 v178, v194, v203, v178
	v_cvt_scalef32_pk_f16_fp4 v197, v14, 1.0 op_sel:[1,1,0]
	v_pk_fma_f16 v179, v195, v203, v179
	v_cvt_scalef32_pk_f16_fp4 v194, v15, 1.0
	v_pk_fma_f16 v180, v196, v203, v180
	v_cvt_scalef32_pk_f16_fp4 v195, v15, 1.0 op_sel:[1,0,0]
	v_pk_fma_f16 v181, v197, v203, v181
	v_cvt_scalef32_pk_f16_fp4 v196, v15, 1.0 op_sel:[0,1,0]
	v_pk_fma_f16 v182, v194, v203, v182
	v_cvt_scalef32_pk_f16_fp4 v197, v15, 1.0 op_sel:[1,1,0]
	v_pk_fma_f16 v183, v195, v203, v183
	v_cvt_scalef32_pk_f16_fp4 v194, v16, 1.0
	v_pk_fma_f16 v184, v196, v203, v184
	v_cvt_scalef32_pk_f16_fp4 v195, v16, 1.0 op_sel:[1,0,0]
	v_pk_fma_f16 v185, v197, v203, v185
	v_cvt_scalef32_pk_f16_fp4 v196, v16, 1.0 op_sel:[0,1,0]
	v_pk_fma_f16 v186, v194, v203, v186
	v_cvt_scalef32_pk_f16_fp4 v197, v16, 1.0 op_sel:[1,1,0]
	v_pk_fma_f16 v187, v195, v203, v187
	v_cvt_scalef32_pk_f16_fp4 v194, v17, 1.0
	v_pk_fma_f16 v188, v196, v203, v188
	v_cvt_scalef32_pk_f16_fp4 v195, v17, 1.0 op_sel:[1,0,0]
	v_pk_fma_f16 v189, v197, v203, v189
	v_cvt_scalef32_pk_f16_fp4 v196, v17, 1.0 op_sel:[0,1,0]
	v_pk_fma_f16 v190, v194, v203, v190
	v_cvt_scalef32_pk_f16_fp4 v197, v17, 1.0 op_sel:[1,1,0]
	v_pk_fma_f16 v191, v195, v203, v191
	v_pk_fma_f16 v192, v196, v203, v192
	v_pk_fma_f16 v193, v197, v203, v193
	v_mul_u32_u24_sdwa v202, v132, s93 dst_sel:DWORD dst_unused:UNUSED_PAD src0_sel:WORD_0 src1_sel:DWORD
	v_cvt_scalef32_pk_f16_fp4 v194, v18, 1.0
	v_cvt_scalef32_pk_f16_fp4 v195, v18, 1.0 op_sel:[1,0,0]
	v_cvt_scalef32_pk_f16_fp4 v196, v18, 1.0 op_sel:[0,1,0]
	v_pk_fma_f16 v178, v194, v202, v178
	v_cvt_scalef32_pk_f16_fp4 v197, v18, 1.0 op_sel:[1,1,0]
	v_pk_fma_f16 v179, v195, v202, v179
	v_cvt_scalef32_pk_f16_fp4 v194, v19, 1.0
	v_pk_fma_f16 v180, v196, v202, v180
	v_cvt_scalef32_pk_f16_fp4 v195, v19, 1.0 op_sel:[1,0,0]
	v_pk_fma_f16 v181, v197, v202, v181
	v_cvt_scalef32_pk_f16_fp4 v196, v19, 1.0 op_sel:[0,1,0]
	v_pk_fma_f16 v182, v194, v202, v182
	v_cvt_scalef32_pk_f16_fp4 v197, v19, 1.0 op_sel:[1,1,0]
	v_pk_fma_f16 v183, v195, v202, v183
	v_cvt_scalef32_pk_f16_fp4 v194, v20, 1.0
	v_pk_fma_f16 v184, v196, v202, v184
	v_cvt_scalef32_pk_f16_fp4 v195, v20, 1.0 op_sel:[1,0,0]
	v_pk_fma_f16 v185, v197, v202, v185
	v_cvt_scalef32_pk_f16_fp4 v196, v20, 1.0 op_sel:[0,1,0]
	v_pk_fma_f16 v186, v194, v202, v186
	v_cvt_scalef32_pk_f16_fp4 v197, v20, 1.0 op_sel:[1,1,0]
	v_pk_fma_f16 v187, v195, v202, v187
	v_cvt_scalef32_pk_f16_fp4 v194, v21, 1.0
	v_pk_fma_f16 v188, v196, v202, v188
	v_cvt_scalef32_pk_f16_fp4 v195, v21, 1.0 op_sel:[1,0,0]
	v_pk_fma_f16 v189, v197, v202, v189
	v_cvt_scalef32_pk_f16_fp4 v196, v21, 1.0 op_sel:[0,1,0]
	v_pk_fma_f16 v190, v194, v202, v190
	v_cvt_scalef32_pk_f16_fp4 v197, v21, 1.0 op_sel:[1,1,0]
	v_pk_fma_f16 v191, v195, v202, v191
	v_pk_fma_f16 v192, v196, v202, v192
	v_pk_fma_f16 v193, v197, v202, v193
	v_mul_u32_u24_sdwa v203, v132, s93 dst_sel:DWORD dst_unused:UNUSED_PAD src0_sel:WORD_1 src1_sel:DWORD
	v_cvt_scalef32_pk_f16_fp4 v194, v22, 1.0
	v_cvt_scalef32_pk_f16_fp4 v195, v22, 1.0 op_sel:[1,0,0]
	v_cvt_scalef32_pk_f16_fp4 v196, v22, 1.0 op_sel:[0,1,0]
	v_pk_fma_f16 v178, v194, v203, v178
	v_cvt_scalef32_pk_f16_fp4 v197, v22, 1.0 op_sel:[1,1,0]
	v_pk_fma_f16 v179, v195, v203, v179
	v_cvt_scalef32_pk_f16_fp4 v194, v23, 1.0
	v_pk_fma_f16 v180, v196, v203, v180
	v_cvt_scalef32_pk_f16_fp4 v195, v23, 1.0 op_sel:[1,0,0]
	v_pk_fma_f16 v181, v197, v203, v181
	v_cvt_scalef32_pk_f16_fp4 v196, v23, 1.0 op_sel:[0,1,0]
	v_pk_fma_f16 v182, v194, v203, v182
	v_cvt_scalef32_pk_f16_fp4 v197, v23, 1.0 op_sel:[1,1,0]
	v_pk_fma_f16 v183, v195, v203, v183
	v_cvt_scalef32_pk_f16_fp4 v194, v24, 1.0
	v_pk_fma_f16 v184, v196, v203, v184
	v_cvt_scalef32_pk_f16_fp4 v195, v24, 1.0 op_sel:[1,0,0]
	v_pk_fma_f16 v185, v197, v203, v185
	v_cvt_scalef32_pk_f16_fp4 v196, v24, 1.0 op_sel:[0,1,0]
	v_pk_fma_f16 v186, v194, v203, v186
	v_cvt_scalef32_pk_f16_fp4 v197, v24, 1.0 op_sel:[1,1,0]
	v_pk_fma_f16 v187, v195, v203, v187
	v_cvt_scalef32_pk_f16_fp4 v194, v25, 1.0
	v_pk_fma_f16 v188, v196, v203, v188
	v_cvt_scalef32_pk_f16_fp4 v195, v25, 1.0 op_sel:[1,0,0]
	v_pk_fma_f16 v189, v197, v203, v189
	v_cvt_scalef32_pk_f16_fp4 v196, v25, 1.0 op_sel:[0,1,0]
	v_pk_fma_f16 v190, v194, v203, v190
	v_cvt_scalef32_pk_f16_fp4 v197, v25, 1.0 op_sel:[1,1,0]
	v_pk_fma_f16 v191, v195, v203, v191
	v_pk_fma_f16 v192, v196, v203, v192
	v_pk_fma_f16 v193, v197, v203, v193
	v_mul_u32_u24_sdwa v202, v133, s93 dst_sel:DWORD dst_unused:UNUSED_PAD src0_sel:WORD_0 src1_sel:DWORD
	v_cvt_scalef32_pk_f16_fp4 v194, v26, 1.0
	v_cvt_scalef32_pk_f16_fp4 v195, v26, 1.0 op_sel:[1,0,0]
	v_cvt_scalef32_pk_f16_fp4 v196, v26, 1.0 op_sel:[0,1,0]
	v_pk_fma_f16 v178, v194, v202, v178
	v_cvt_scalef32_pk_f16_fp4 v197, v26, 1.0 op_sel:[1,1,0]
	v_pk_fma_f16 v179, v195, v202, v179
	v_cvt_scalef32_pk_f16_fp4 v194, v27, 1.0
	v_pk_fma_f16 v180, v196, v202, v180
	v_cvt_scalef32_pk_f16_fp4 v195, v27, 1.0 op_sel:[1,0,0]
	v_pk_fma_f16 v181, v197, v202, v181
	v_cvt_scalef32_pk_f16_fp4 v196, v27, 1.0 op_sel:[0,1,0]
	v_pk_fma_f16 v182, v194, v202, v182
	v_cvt_scalef32_pk_f16_fp4 v197, v27, 1.0 op_sel:[1,1,0]
	v_pk_fma_f16 v183, v195, v202, v183
	v_cvt_scalef32_pk_f16_fp4 v194, v28, 1.0
	v_pk_fma_f16 v184, v196, v202, v184
	v_cvt_scalef32_pk_f16_fp4 v195, v28, 1.0 op_sel:[1,0,0]
	v_pk_fma_f16 v185, v197, v202, v185
	v_cvt_scalef32_pk_f16_fp4 v196, v28, 1.0 op_sel:[0,1,0]
	v_pk_fma_f16 v186, v194, v202, v186
	v_cvt_scalef32_pk_f16_fp4 v197, v28, 1.0 op_sel:[1,1,0]
	v_pk_fma_f16 v187, v195, v202, v187
	v_cvt_scalef32_pk_f16_fp4 v194, v29, 1.0
	v_pk_fma_f16 v188, v196, v202, v188
	v_cvt_scalef32_pk_f16_fp4 v195, v29, 1.0 op_sel:[1,0,0]
	v_pk_fma_f16 v189, v197, v202, v189
	v_cvt_scalef32_pk_f16_fp4 v196, v29, 1.0 op_sel:[0,1,0]
	v_pk_fma_f16 v190, v194, v202, v190
	v_cvt_scalef32_pk_f16_fp4 v197, v29, 1.0 op_sel:[1,1,0]
	v_pk_fma_f16 v191, v195, v202, v191
	v_pk_fma_f16 v192, v196, v202, v192
	v_pk_fma_f16 v193, v197, v202, v193
	v_mul_u32_u24_sdwa v203, v133, s93 dst_sel:DWORD dst_unused:UNUSED_PAD src0_sel:WORD_1 src1_sel:DWORD
	v_cvt_scalef32_pk_f16_fp4 v194, v30, 1.0
	v_cvt_scalef32_pk_f16_fp4 v195, v30, 1.0 op_sel:[1,0,0]
	v_cvt_scalef32_pk_f16_fp4 v196, v30, 1.0 op_sel:[0,1,0]
	v_pk_fma_f16 v178, v194, v203, v178
	v_cvt_scalef32_pk_f16_fp4 v197, v30, 1.0 op_sel:[1,1,0]
	v_pk_fma_f16 v179, v195, v203, v179
	v_cvt_scalef32_pk_f16_fp4 v194, v31, 1.0
	v_pk_fma_f16 v180, v196, v203, v180
	v_cvt_scalef32_pk_f16_fp4 v195, v31, 1.0 op_sel:[1,0,0]
	v_pk_fma_f16 v181, v197, v203, v181
	v_cvt_scalef32_pk_f16_fp4 v196, v31, 1.0 op_sel:[0,1,0]
	v_pk_fma_f16 v182, v194, v203, v182
	v_cvt_scalef32_pk_f16_fp4 v197, v31, 1.0 op_sel:[1,1,0]
	v_pk_fma_f16 v183, v195, v203, v183
	v_cvt_scalef32_pk_f16_fp4 v194, v32, 1.0
	v_pk_fma_f16 v184, v196, v203, v184
	v_cvt_scalef32_pk_f16_fp4 v195, v32, 1.0 op_sel:[1,0,0]
	v_pk_fma_f16 v185, v197, v203, v185
	v_cvt_scalef32_pk_f16_fp4 v196, v32, 1.0 op_sel:[0,1,0]
	v_pk_fma_f16 v186, v194, v203, v186
	v_cvt_scalef32_pk_f16_fp4 v197, v32, 1.0 op_sel:[1,1,0]
	v_pk_fma_f16 v187, v195, v203, v187
	v_cvt_scalef32_pk_f16_fp4 v194, v33, 1.0
	v_pk_fma_f16 v188, v196, v203, v188
	v_cvt_scalef32_pk_f16_fp4 v195, v33, 1.0 op_sel:[1,0,0]
	v_pk_fma_f16 v189, v197, v203, v189
	v_cvt_scalef32_pk_f16_fp4 v196, v33, 1.0 op_sel:[0,1,0]
	v_pk_fma_f16 v190, v194, v203, v190
	v_cvt_scalef32_pk_f16_fp4 v197, v33, 1.0 op_sel:[1,1,0]
	v_pk_fma_f16 v191, v195, v203, v191
	v_pk_fma_f16 v192, v196, v203, v192
	v_pk_fma_f16 v193, v197, v203, v193
	v_mul_u32_u24_sdwa v202, v134, s93 dst_sel:DWORD dst_unused:UNUSED_PAD src0_sel:WORD_0 src1_sel:DWORD
	v_cvt_scalef32_pk_f16_fp4 v194, v34, 1.0
	v_cvt_scalef32_pk_f16_fp4 v195, v34, 1.0 op_sel:[1,0,0]
	v_cvt_scalef32_pk_f16_fp4 v196, v34, 1.0 op_sel:[0,1,0]
	v_pk_fma_f16 v178, v194, v202, v178
	v_cvt_scalef32_pk_f16_fp4 v197, v34, 1.0 op_sel:[1,1,0]
	v_pk_fma_f16 v179, v195, v202, v179
	v_cvt_scalef32_pk_f16_fp4 v194, v35, 1.0
	v_pk_fma_f16 v180, v196, v202, v180
	v_cvt_scalef32_pk_f16_fp4 v195, v35, 1.0 op_sel:[1,0,0]
	v_pk_fma_f16 v181, v197, v202, v181
	v_cvt_scalef32_pk_f16_fp4 v196, v35, 1.0 op_sel:[0,1,0]
	v_pk_fma_f16 v182, v194, v202, v182
	v_cvt_scalef32_pk_f16_fp4 v197, v35, 1.0 op_sel:[1,1,0]
	v_pk_fma_f16 v183, v195, v202, v183
	v_cvt_scalef32_pk_f16_fp4 v194, v36, 1.0
	v_pk_fma_f16 v184, v196, v202, v184
	v_cvt_scalef32_pk_f16_fp4 v195, v36, 1.0 op_sel:[1,0,0]
	v_pk_fma_f16 v185, v197, v202, v185
	v_cvt_scalef32_pk_f16_fp4 v196, v36, 1.0 op_sel:[0,1,0]
	v_pk_fma_f16 v186, v194, v202, v186
	v_cvt_scalef32_pk_f16_fp4 v197, v36, 1.0 op_sel:[1,1,0]
	v_pk_fma_f16 v187, v195, v202, v187
	v_cvt_scalef32_pk_f16_fp4 v194, v37, 1.0
	v_pk_fma_f16 v188, v196, v202, v188
	v_cvt_scalef32_pk_f16_fp4 v195, v37, 1.0 op_sel:[1,0,0]
	v_pk_fma_f16 v189, v197, v202, v189
	v_cvt_scalef32_pk_f16_fp4 v196, v37, 1.0 op_sel:[0,1,0]
	v_pk_fma_f16 v190, v194, v202, v190
	v_cvt_scalef32_pk_f16_fp4 v197, v37, 1.0 op_sel:[1,1,0]
	v_pk_fma_f16 v191, v195, v202, v191
	v_pk_fma_f16 v192, v196, v202, v192
	v_pk_fma_f16 v193, v197, v202, v193
	v_mul_u32_u24_sdwa v203, v134, s93 dst_sel:DWORD dst_unused:UNUSED_PAD src0_sel:WORD_1 src1_sel:DWORD
	v_cvt_scalef32_pk_f16_fp4 v194, v38, 1.0
	v_cvt_scalef32_pk_f16_fp4 v195, v38, 1.0 op_sel:[1,0,0]
	v_cvt_scalef32_pk_f16_fp4 v196, v38, 1.0 op_sel:[0,1,0]
	v_pk_fma_f16 v178, v194, v203, v178
	v_cvt_scalef32_pk_f16_fp4 v197, v38, 1.0 op_sel:[1,1,0]
	v_pk_fma_f16 v179, v195, v203, v179
	v_cvt_scalef32_pk_f16_fp4 v194, v39, 1.0
	v_pk_fma_f16 v180, v196, v203, v180
	v_cvt_scalef32_pk_f16_fp4 v195, v39, 1.0 op_sel:[1,0,0]
	v_pk_fma_f16 v181, v197, v203, v181
	v_cvt_scalef32_pk_f16_fp4 v196, v39, 1.0 op_sel:[0,1,0]
	v_pk_fma_f16 v182, v194, v203, v182
	v_cvt_scalef32_pk_f16_fp4 v197, v39, 1.0 op_sel:[1,1,0]
	v_pk_fma_f16 v183, v195, v203, v183
	v_cvt_scalef32_pk_f16_fp4 v194, v40, 1.0
	v_pk_fma_f16 v184, v196, v203, v184
	v_cvt_scalef32_pk_f16_fp4 v195, v40, 1.0 op_sel:[1,0,0]
	v_pk_fma_f16 v185, v197, v203, v185
	v_cvt_scalef32_pk_f16_fp4 v196, v40, 1.0 op_sel:[0,1,0]
	v_pk_fma_f16 v186, v194, v203, v186
	v_cvt_scalef32_pk_f16_fp4 v197, v40, 1.0 op_sel:[1,1,0]
	v_pk_fma_f16 v187, v195, v203, v187
	v_cvt_scalef32_pk_f16_fp4 v194, v41, 1.0
	v_pk_fma_f16 v188, v196, v203, v188
	v_cvt_scalef32_pk_f16_fp4 v195, v41, 1.0 op_sel:[1,0,0]
	v_pk_fma_f16 v189, v197, v203, v189
	v_cvt_scalef32_pk_f16_fp4 v196, v41, 1.0 op_sel:[0,1,0]
	v_pk_fma_f16 v190, v194, v203, v190
	v_cvt_scalef32_pk_f16_fp4 v197, v41, 1.0 op_sel:[1,1,0]
	v_pk_fma_f16 v191, v195, v203, v191
	v_pk_fma_f16 v192, v196, v203, v192
	v_pk_fma_f16 v193, v197, v203, v193
	v_mul_u32_u24_sdwa v202, v135, s93 dst_sel:DWORD dst_unused:UNUSED_PAD src0_sel:WORD_0 src1_sel:DWORD
	v_cvt_scalef32_pk_f16_fp4 v194, v42, 1.0
	v_cvt_scalef32_pk_f16_fp4 v195, v42, 1.0 op_sel:[1,0,0]
	v_cvt_scalef32_pk_f16_fp4 v196, v42, 1.0 op_sel:[0,1,0]
	v_pk_fma_f16 v178, v194, v202, v178
	v_cvt_scalef32_pk_f16_fp4 v197, v42, 1.0 op_sel:[1,1,0]
	v_pk_fma_f16 v179, v195, v202, v179
	v_cvt_scalef32_pk_f16_fp4 v194, v43, 1.0
	v_pk_fma_f16 v180, v196, v202, v180
	v_cvt_scalef32_pk_f16_fp4 v195, v43, 1.0 op_sel:[1,0,0]
	v_pk_fma_f16 v181, v197, v202, v181
	v_cvt_scalef32_pk_f16_fp4 v196, v43, 1.0 op_sel:[0,1,0]
	v_pk_fma_f16 v182, v194, v202, v182
	v_cvt_scalef32_pk_f16_fp4 v197, v43, 1.0 op_sel:[1,1,0]
	v_pk_fma_f16 v183, v195, v202, v183
	v_cvt_scalef32_pk_f16_fp4 v194, v44, 1.0
	v_pk_fma_f16 v184, v196, v202, v184
	v_cvt_scalef32_pk_f16_fp4 v195, v44, 1.0 op_sel:[1,0,0]
	v_pk_fma_f16 v185, v197, v202, v185
	v_cvt_scalef32_pk_f16_fp4 v196, v44, 1.0 op_sel:[0,1,0]
	v_pk_fma_f16 v186, v194, v202, v186
	v_cvt_scalef32_pk_f16_fp4 v197, v44, 1.0 op_sel:[1,1,0]
	v_pk_fma_f16 v187, v195, v202, v187
	v_cvt_scalef32_pk_f16_fp4 v194, v45, 1.0
	v_pk_fma_f16 v188, v196, v202, v188
	v_cvt_scalef32_pk_f16_fp4 v195, v45, 1.0 op_sel:[1,0,0]
	v_pk_fma_f16 v189, v197, v202, v189
	v_cvt_scalef32_pk_f16_fp4 v196, v45, 1.0 op_sel:[0,1,0]
	v_pk_fma_f16 v190, v194, v202, v190
	v_cvt_scalef32_pk_f16_fp4 v197, v45, 1.0 op_sel:[1,1,0]
	v_pk_fma_f16 v191, v195, v202, v191
	v_pk_fma_f16 v192, v196, v202, v192
	v_pk_fma_f16 v193, v197, v202, v193
	v_mul_u32_u24_sdwa v203, v135, s93 dst_sel:DWORD dst_unused:UNUSED_PAD src0_sel:WORD_1 src1_sel:DWORD
	v_cvt_scalef32_pk_f16_fp4 v194, v46, 1.0
	v_cvt_scalef32_pk_f16_fp4 v195, v46, 1.0 op_sel:[1,0,0]
	v_cvt_scalef32_pk_f16_fp4 v196, v46, 1.0 op_sel:[0,1,0]
	v_pk_fma_f16 v178, v194, v203, v178
	v_cvt_scalef32_pk_f16_fp4 v197, v46, 1.0 op_sel:[1,1,0]
	v_pk_fma_f16 v179, v195, v203, v179
	v_cvt_scalef32_pk_f16_fp4 v194, v47, 1.0
	v_pk_fma_f16 v180, v196, v203, v180
	v_cvt_scalef32_pk_f16_fp4 v195, v47, 1.0 op_sel:[1,0,0]
	v_pk_fma_f16 v181, v197, v203, v181
	v_cvt_scalef32_pk_f16_fp4 v196, v47, 1.0 op_sel:[0,1,0]
	v_pk_fma_f16 v182, v194, v203, v182
	v_cvt_scalef32_pk_f16_fp4 v197, v47, 1.0 op_sel:[1,1,0]
	v_pk_fma_f16 v183, v195, v203, v183
	v_cvt_scalef32_pk_f16_fp4 v194, v48, 1.0
	v_pk_fma_f16 v184, v196, v203, v184
	v_cvt_scalef32_pk_f16_fp4 v195, v48, 1.0 op_sel:[1,0,0]
	v_pk_fma_f16 v185, v197, v203, v185
	v_cvt_scalef32_pk_f16_fp4 v196, v48, 1.0 op_sel:[0,1,0]
	v_pk_fma_f16 v186, v194, v203, v186
	v_cvt_scalef32_pk_f16_fp4 v197, v48, 1.0 op_sel:[1,1,0]
	v_pk_fma_f16 v187, v195, v203, v187
	v_cvt_scalef32_pk_f16_fp4 v194, v49, 1.0
	v_pk_fma_f16 v188, v196, v203, v188
	v_cvt_scalef32_pk_f16_fp4 v195, v49, 1.0 op_sel:[1,0,0]
	v_pk_fma_f16 v189, v197, v203, v189
	v_cvt_scalef32_pk_f16_fp4 v196, v49, 1.0 op_sel:[0,1,0]
	v_pk_fma_f16 v190, v194, v203, v190
	v_cvt_scalef32_pk_f16_fp4 v197, v49, 1.0 op_sel:[1,1,0]
	v_pk_fma_f16 v191, v195, v203, v191
	v_pk_fma_f16 v192, v196, v203, v192
	v_pk_fma_f16 v193, v197, v203, v193
	v_mul_u32_u24_sdwa v202, v136, s93 dst_sel:DWORD dst_unused:UNUSED_PAD src0_sel:WORD_0 src1_sel:DWORD
	v_cvt_scalef32_pk_f16_fp4 v194, v50, 1.0
	v_cvt_scalef32_pk_f16_fp4 v195, v50, 1.0 op_sel:[1,0,0]
	v_cvt_scalef32_pk_f16_fp4 v196, v50, 1.0 op_sel:[0,1,0]
	v_pk_fma_f16 v178, v194, v202, v178
	v_cvt_scalef32_pk_f16_fp4 v197, v50, 1.0 op_sel:[1,1,0]
	v_pk_fma_f16 v179, v195, v202, v179
	v_cvt_scalef32_pk_f16_fp4 v194, v51, 1.0
	v_pk_fma_f16 v180, v196, v202, v180
	v_cvt_scalef32_pk_f16_fp4 v195, v51, 1.0 op_sel:[1,0,0]
	v_pk_fma_f16 v181, v197, v202, v181
	v_cvt_scalef32_pk_f16_fp4 v196, v51, 1.0 op_sel:[0,1,0]
	v_pk_fma_f16 v182, v194, v202, v182
	v_cvt_scalef32_pk_f16_fp4 v197, v51, 1.0 op_sel:[1,1,0]
	v_pk_fma_f16 v183, v195, v202, v183
	v_cvt_scalef32_pk_f16_fp4 v194, v52, 1.0
	v_pk_fma_f16 v184, v196, v202, v184
	v_cvt_scalef32_pk_f16_fp4 v195, v52, 1.0 op_sel:[1,0,0]
	v_pk_fma_f16 v185, v197, v202, v185
	v_cvt_scalef32_pk_f16_fp4 v196, v52, 1.0 op_sel:[0,1,0]
	v_pk_fma_f16 v186, v194, v202, v186
	v_cvt_scalef32_pk_f16_fp4 v197, v52, 1.0 op_sel:[1,1,0]
	v_pk_fma_f16 v187, v195, v202, v187
	v_cvt_scalef32_pk_f16_fp4 v194, v53, 1.0
	v_pk_fma_f16 v188, v196, v202, v188
	v_cvt_scalef32_pk_f16_fp4 v195, v53, 1.0 op_sel:[1,0,0]
	v_pk_fma_f16 v189, v197, v202, v189
	v_cvt_scalef32_pk_f16_fp4 v196, v53, 1.0 op_sel:[0,1,0]
	v_pk_fma_f16 v190, v194, v202, v190
	v_cvt_scalef32_pk_f16_fp4 v197, v53, 1.0 op_sel:[1,1,0]
	v_pk_fma_f16 v191, v195, v202, v191
	v_pk_fma_f16 v192, v196, v202, v192
	v_pk_fma_f16 v193, v197, v202, v193
	v_mul_u32_u24_sdwa v203, v136, s93 dst_sel:DWORD dst_unused:UNUSED_PAD src0_sel:WORD_1 src1_sel:DWORD
	v_cvt_scalef32_pk_f16_fp4 v194, v54, 1.0
	v_cvt_scalef32_pk_f16_fp4 v195, v54, 1.0 op_sel:[1,0,0]
	v_cvt_scalef32_pk_f16_fp4 v196, v54, 1.0 op_sel:[0,1,0]
	v_pk_fma_f16 v178, v194, v203, v178
	v_cvt_scalef32_pk_f16_fp4 v197, v54, 1.0 op_sel:[1,1,0]
	v_pk_fma_f16 v179, v195, v203, v179
	v_cvt_scalef32_pk_f16_fp4 v194, v55, 1.0
	v_pk_fma_f16 v180, v196, v203, v180
	v_cvt_scalef32_pk_f16_fp4 v195, v55, 1.0 op_sel:[1,0,0]
	v_pk_fma_f16 v181, v197, v203, v181
	v_cvt_scalef32_pk_f16_fp4 v196, v55, 1.0 op_sel:[0,1,0]
	v_pk_fma_f16 v182, v194, v203, v182
	v_cvt_scalef32_pk_f16_fp4 v197, v55, 1.0 op_sel:[1,1,0]
	v_pk_fma_f16 v183, v195, v203, v183
	v_cvt_scalef32_pk_f16_fp4 v194, v56, 1.0
	v_pk_fma_f16 v184, v196, v203, v184
	v_cvt_scalef32_pk_f16_fp4 v195, v56, 1.0 op_sel:[1,0,0]
	v_pk_fma_f16 v185, v197, v203, v185
	v_cvt_scalef32_pk_f16_fp4 v196, v56, 1.0 op_sel:[0,1,0]
	v_pk_fma_f16 v186, v194, v203, v186
	v_cvt_scalef32_pk_f16_fp4 v197, v56, 1.0 op_sel:[1,1,0]
	v_pk_fma_f16 v187, v195, v203, v187
	v_cvt_scalef32_pk_f16_fp4 v194, v57, 1.0
	v_pk_fma_f16 v188, v196, v203, v188
	v_cvt_scalef32_pk_f16_fp4 v195, v57, 1.0 op_sel:[1,0,0]
	v_pk_fma_f16 v189, v197, v203, v189
	v_cvt_scalef32_pk_f16_fp4 v196, v57, 1.0 op_sel:[0,1,0]
	v_pk_fma_f16 v190, v194, v203, v190
	v_cvt_scalef32_pk_f16_fp4 v197, v57, 1.0 op_sel:[1,1,0]
	v_pk_fma_f16 v191, v195, v203, v191
	v_pk_fma_f16 v192, v196, v203, v192
	v_pk_fma_f16 v193, v197, v203, v193
	v_mul_u32_u24_sdwa v202, v137, s93 dst_sel:DWORD dst_unused:UNUSED_PAD src0_sel:WORD_0 src1_sel:DWORD
	v_cvt_scalef32_pk_f16_fp4 v194, v58, 1.0
	v_cvt_scalef32_pk_f16_fp4 v195, v58, 1.0 op_sel:[1,0,0]
	v_cvt_scalef32_pk_f16_fp4 v196, v58, 1.0 op_sel:[0,1,0]
	v_pk_fma_f16 v178, v194, v202, v178
	v_cvt_scalef32_pk_f16_fp4 v197, v58, 1.0 op_sel:[1,1,0]
	v_pk_fma_f16 v179, v195, v202, v179
	v_cvt_scalef32_pk_f16_fp4 v194, v59, 1.0
	v_pk_fma_f16 v180, v196, v202, v180
	v_cvt_scalef32_pk_f16_fp4 v195, v59, 1.0 op_sel:[1,0,0]
	v_pk_fma_f16 v181, v197, v202, v181
	v_cvt_scalef32_pk_f16_fp4 v196, v59, 1.0 op_sel:[0,1,0]
	v_pk_fma_f16 v182, v194, v202, v182
	v_cvt_scalef32_pk_f16_fp4 v197, v59, 1.0 op_sel:[1,1,0]
	v_pk_fma_f16 v183, v195, v202, v183
	v_cvt_scalef32_pk_f16_fp4 v194, v60, 1.0
	v_pk_fma_f16 v184, v196, v202, v184
	v_cvt_scalef32_pk_f16_fp4 v195, v60, 1.0 op_sel:[1,0,0]
	v_pk_fma_f16 v185, v197, v202, v185
	v_cvt_scalef32_pk_f16_fp4 v196, v60, 1.0 op_sel:[0,1,0]
	v_pk_fma_f16 v186, v194, v202, v186
	v_cvt_scalef32_pk_f16_fp4 v197, v60, 1.0 op_sel:[1,1,0]
	v_pk_fma_f16 v187, v195, v202, v187
	v_cvt_scalef32_pk_f16_fp4 v194, v61, 1.0
	v_pk_fma_f16 v188, v196, v202, v188
	v_cvt_scalef32_pk_f16_fp4 v195, v61, 1.0 op_sel:[1,0,0]
	v_pk_fma_f16 v189, v197, v202, v189
	v_cvt_scalef32_pk_f16_fp4 v196, v61, 1.0 op_sel:[0,1,0]
	v_pk_fma_f16 v190, v194, v202, v190
	v_cvt_scalef32_pk_f16_fp4 v197, v61, 1.0 op_sel:[1,1,0]
	v_pk_fma_f16 v191, v195, v202, v191
	v_pk_fma_f16 v192, v196, v202, v192
	v_pk_fma_f16 v193, v197, v202, v193
	v_mul_u32_u24_sdwa v203, v137, s93 dst_sel:DWORD dst_unused:UNUSED_PAD src0_sel:WORD_1 src1_sel:DWORD
	v_cvt_scalef32_pk_f16_fp4 v194, v62, 1.0
	v_cvt_scalef32_pk_f16_fp4 v195, v62, 1.0 op_sel:[1,0,0]
	v_cvt_scalef32_pk_f16_fp4 v196, v62, 1.0 op_sel:[0,1,0]
	v_pk_fma_f16 v178, v194, v203, v178
	v_cvt_scalef32_pk_f16_fp4 v197, v62, 1.0 op_sel:[1,1,0]
	v_pk_fma_f16 v179, v195, v203, v179
	v_cvt_scalef32_pk_f16_fp4 v194, v63, 1.0
	v_pk_fma_f16 v180, v196, v203, v180
	v_cvt_scalef32_pk_f16_fp4 v195, v63, 1.0 op_sel:[1,0,0]
	v_pk_fma_f16 v181, v197, v203, v181
	v_cvt_scalef32_pk_f16_fp4 v196, v63, 1.0 op_sel:[0,1,0]
	v_pk_fma_f16 v182, v194, v203, v182
	v_cvt_scalef32_pk_f16_fp4 v197, v63, 1.0 op_sel:[1,1,0]
	v_pk_fma_f16 v183, v195, v203, v183
	v_cvt_scalef32_pk_f16_fp4 v194, v64, 1.0
	v_pk_fma_f16 v184, v196, v203, v184
	v_cvt_scalef32_pk_f16_fp4 v195, v64, 1.0 op_sel:[1,0,0]
	v_pk_fma_f16 v185, v197, v203, v185
	v_cvt_scalef32_pk_f16_fp4 v196, v64, 1.0 op_sel:[0,1,0]
	v_pk_fma_f16 v186, v194, v203, v186
	v_cvt_scalef32_pk_f16_fp4 v197, v64, 1.0 op_sel:[1,1,0]
	v_pk_fma_f16 v187, v195, v203, v187
	v_cvt_scalef32_pk_f16_fp4 v194, v65, 1.0
	v_pk_fma_f16 v188, v196, v203, v188
	v_cvt_scalef32_pk_f16_fp4 v195, v65, 1.0 op_sel:[1,0,0]
	v_pk_fma_f16 v189, v197, v203, v189
	v_cvt_scalef32_pk_f16_fp4 v196, v65, 1.0 op_sel:[0,1,0]
	v_pk_fma_f16 v190, v194, v203, v190
	v_cvt_scalef32_pk_f16_fp4 v197, v65, 1.0 op_sel:[1,1,0]
	v_pk_fma_f16 v191, v195, v203, v191
	v_pk_fma_f16 v192, v196, v203, v192
	v_pk_fma_f16 v193, v197, v203, v193
	s_nop 1
	v_permlane32_swap_b32_e32 v178, v186
	v_permlane32_swap_b32_e32 v179, v187
	v_permlane32_swap_b32_e32 v180, v188
	v_permlane32_swap_b32_e32 v181, v189
	v_permlane32_swap_b32_e32 v182, v190
	v_permlane32_swap_b32_e32 v183, v191
	v_permlane32_swap_b32_e32 v184, v192
	v_permlane32_swap_b32_e32 v185, v193
	v_pk_add_f16 v2, v178, v186
	v_pk_add_f16 v3, v179, v187
	v_pk_add_f16 v4, v180, v188
	v_pk_add_f16 v5, v181, v189
	v_pk_add_f16 v6, v182, v190
	v_pk_add_f16 v7, v183, v191
	v_pk_add_f16 v8, v184, v192
	v_pk_add_f16 v9, v185, v193
	v_cvt_f32_f16_e32 v10, v2
	v_cvt_f32_f16_sdwa v11, v2 dst_sel:DWORD dst_unused:UNUSED_PAD src0_sel:WORD_1
	v_cvt_f32_f16_e32 v12, v3
	v_cvt_f32_f16_sdwa v13, v3 dst_sel:DWORD dst_unused:UNUSED_PAD src0_sel:WORD_1
	v_cvt_f32_f16_e32 v14, v4
	v_cvt_f32_f16_sdwa v15, v4 dst_sel:DWORD dst_unused:UNUSED_PAD src0_sel:WORD_1
	v_cvt_f32_f16_e32 v16, v5
	v_cvt_f32_f16_sdwa v17, v5 dst_sel:DWORD dst_unused:UNUSED_PAD src0_sel:WORD_1
	v_cvt_f32_f16_e32 v18, v6
	v_cvt_f32_f16_sdwa v19, v6 dst_sel:DWORD dst_unused:UNUSED_PAD src0_sel:WORD_1
	v_cvt_f32_f16_e32 v20, v7
	v_cvt_f32_f16_sdwa v21, v7 dst_sel:DWORD dst_unused:UNUSED_PAD src0_sel:WORD_1
	v_cvt_f32_f16_e32 v22, v8
	v_cvt_f32_f16_sdwa v23, v8 dst_sel:DWORD dst_unused:UNUSED_PAD src0_sel:WORD_1
	v_cvt_f32_f16_e32 v24, v9
	v_cvt_f32_f16_sdwa v25, v9 dst_sel:DWORD dst_unused:UNUSED_PAD src0_sel:WORD_1
	s_nop 1
	v_permlane16_swap_b32_e32 v10, v18
	v_permlane16_swap_b32_e32 v11, v19
	v_permlane16_swap_b32_e32 v12, v20
	v_permlane16_swap_b32_e32 v13, v21
	v_permlane16_swap_b32_e32 v14, v22
	v_permlane16_swap_b32_e32 v15, v23
	v_permlane16_swap_b32_e32 v16, v24
	v_permlane16_swap_b32_e32 v17, v25
	v_add_f32_e32 v26, v10, v18
	v_add_f32_e32 v27, v11, v19
	v_add_f32_e32 v28, v12, v20
	v_add_f32_e32 v29, v13, v21
	v_add_f32_e32 v30, v14, v22
	v_add_f32_e32 v31, v15, v23
	v_add_f32_e32 v32, v16, v24
	v_add_f32_e32 v33, v17, v25
	s_nop 1
	v_add_f32_dpp v34, v26, v26 row_ror:8 row_mask:0xf bank_mask:0xf bound_ctrl:1
	v_add_f32_dpp v35, v30, v30 row_ror:8 row_mask:0xf bank_mask:0xf bound_ctrl:1
	v_add_f32_dpp v36, v27, v27 row_ror:8 row_mask:0xf bank_mask:0xf bound_ctrl:1
	v_add_f32_dpp v37, v31, v31 row_ror:8 row_mask:0xf bank_mask:0xf bound_ctrl:1
	v_add_f32_dpp v38, v28, v28 row_ror:8 row_mask:0xf bank_mask:0xf bound_ctrl:1
	v_add_f32_dpp v39, v32, v32 row_ror:8 row_mask:0xf bank_mask:0xf bound_ctrl:1
	v_add_f32_dpp v40, v29, v29 row_ror:8 row_mask:0xf bank_mask:0xf bound_ctrl:1
	v_add_f32_dpp v41, v33, v33 row_ror:8 row_mask:0xf bank_mask:0xf bound_ctrl:1
	v_cndmask_b32_e64 v42, v35, v34, s[38:39]
	v_cndmask_b32_e64 v43, v37, v36, s[38:39]
	v_cndmask_b32_e64 v44, v39, v38, s[38:39]
	v_cndmask_b32_e64 v45, v41, v40, s[38:39]
	v_fma_f32 v46, v150, v42, v146
	v_fma_f32 v47, v151, v43, v147
	v_fma_f32 v48, v152, v44, v148
	v_fma_f32 v49, v153, v45, v149
	global_store_dwordx4 v[238:239], v[46:49], off
	s_waitcnt vmcnt(1)
	s_cmp_lt_u32 s33, 6
	s_cbranch_scc0 .Le2_skipB
	v_and_b32_e32 v194, 0xffff, v162
	v_lshrrev_b32_e32 v195, 16, v162
	v_lshl_add_u32 v194, v194, 7, v218
	v_lshl_add_u32 v195, v195, 7, v218
	global_load_dwordx4 v[2:5], v194, s[40:41]
	global_load_dwordx4 v[6:9], v195, s[40:41]
	v_and_b32_e32 v194, 0xffff, v163
	v_lshrrev_b32_e32 v195, 16, v163
	v_lshl_add_u32 v194, v194, 7, v218
	v_lshl_add_u32 v195, v195, 7, v218
	global_load_dwordx4 v[10:13], v194, s[40:41]
	global_load_dwordx4 v[14:17], v195, s[40:41]
	v_and_b32_e32 v194, 0xffff, v164
	v_lshrrev_b32_e32 v195, 16, v164
	v_lshl_add_u32 v194, v194, 7, v218
	v_lshl_add_u32 v195, v195, 7, v218
	global_load_dwordx4 v[18:21], v194, s[40:41]
	global_load_dwordx4 v[22:25], v195, s[40:41]
	v_and_b32_e32 v194, 0xffff, v165
	v_lshrrev_b32_e32 v195, 16, v165
	v_lshl_add_u32 v194, v194, 7, v218
	v_lshl_add_u32 v195, v195, 7, v218
	global_load_dwordx4 v[26:29], v194, s[40:41]
	global_load_dwordx4 v[30:33], v195, s[40:41]
	v_and_b32_e32 v194, 0xffff, v166
	v_lshrrev_b32_e32 v195, 16, v166
	v_lshl_add_u32 v194, v194, 7, v218
	v_lshl_add_u32 v195, v195, 7, v218
	global_load_dwordx4 v[34:37], v194, s[40:41]
	global_load_dwordx4 v[38:41], v195, s[40:41]
	v_and_b32_e32 v194, 0xffff, v167
	v_lshrrev_b32_e32 v195, 16, v167
	v_lshl_add_u32 v194, v194, 7, v218
	v_lshl_add_u32 v195, v195, 7, v218
	global_load_dwordx4 v[42:45], v194, s[40:41]
	global_load_dwordx4 v[46:49], v195, s[40:41]
	v_and_b32_e32 v194, 0xffff, v168
	v_lshrrev_b32_e32 v195, 16, v168
	v_lshl_add_u32 v194, v194, 7, v218
	v_lshl_add_u32 v195, v195, 7, v218
	global_load_dwordx4 v[50:53], v194, s[40:41]
	global_load_dwordx4 v[54:57], v195, s[40:41]
	v_and_b32_e32 v194, 0xffff, v169
	v_lshrrev_b32_e32 v195, 16, v169
	v_lshl_add_u32 v194, v194, 7, v218
	v_lshl_add_u32 v195, v195, 7, v218
	global_load_dwordx4 v[58:61], v194, s[40:41]
	global_load_dwordx4 v[62:65], v195, s[40:41]
	global_load_dwordx4 v[130:133], v219, s[56:57] offset:-272
	global_load_dwordx4 v[134:137], v219, s[56:57] offset:-256
	v_add_u32_e32 v250, 2, v226
	v_mul_hi_i32 v242, v250, s69
	v_lshrrev_b32_e32 v243, 31, v242
	v_ashrrev_i32_e32 v242, 13, v242
	v_add_u32_e32 v243, v242, v243
	v_mul_i32_i24_e32 v246, 0xffffbf00, v243
	v_add_u32_e32 v242, v250, v246
	v_cmp_gt_i32_e32 vcc, s68, v242
	v_cmp_lt_i32_e64 s[0:1], s21, v242
	s_and_saveexec_b64 s[2:3], s[0:1]
	s_xor_b64 s[0:1], exec, s[2:3]
	v_lshl_add_u32 v242, v243, 14, v246
	v_add3_u32 v242, v250, v242, s88
	s_or_saveexec_b64 s[0:1], s[0:1]
	v_mov_b64_e32 v[244:245], s[18:19]
	s_xor_b64 exec, exec, s[0:1]
	v_lshlrev_b32_e32 v242, 8, v243
	v_add3_u32 v242, v246, v250, v242
	v_mov_b64_e32 v[244:245], s[72:73]
	s_or_b64 exec, exec, s[0:1]
	v_mul_i32_i24_e32 v243, 0x3000, v243
	v_cndmask_b32_e32 v246, v243, v223, vcc
	v_ashrrev_i32_e32 v247, 31, v246
	v_lshl_add_u64 v[246:247], v[246:247], 2, s[10:11]
	v_ashrrev_i32_e32 v243, 31, v242
	v_lshl_add_u64 v[248:249], v[246:247], 0, v[236:237]
	v_lshlrev_b64 v[242:243], 13, v[242:243]
	v_lshl_add_u64 v[242:243], v[244:245], 0, v[242:243]
	v_add_co_u32_e32 v248, vcc, s94, v248
	v_lshl_add_u64 v[238:239], v[242:243], 0, v[236:237]
	s_nop 0
	v_addc_co_u32_e32 v249, vcc, 0, v249, vcc
	global_load_dwordx4 v[146:149], v[238:239], off
	global_load_dwordx4 v[150:153], v[248:249], off
	global_load_dwordx4 v[170:173], v219, s[22:23] offset:256
	global_load_dwordx4 v[174:177], v219, s[22:23] offset:272
	v_add_u32_e32 v219, 0x200, v219
.Le2_skipB:
	v_mul_u32_u24_sdwa v202, v138, s93 dst_sel:DWORD dst_unused:UNUSED_PAD src0_sel:WORD_0 src1_sel:DWORD
	v_cvt_scalef32_pk_f16_fp4 v194, v66, 1.0
	v_cvt_scalef32_pk_f16_fp4 v195, v66, 1.0 op_sel:[1,0,0]
	v_cvt_scalef32_pk_f16_fp4 v196, v66, 1.0 op_sel:[0,1,0]
	v_pk_fma_f16 v178, v194, v202, 0
	v_cvt_scalef32_pk_f16_fp4 v197, v66, 1.0 op_sel:[1,1,0]
	v_pk_fma_f16 v179, v195, v202, 0
	v_cvt_scalef32_pk_f16_fp4 v194, v67, 1.0
	v_pk_fma_f16 v180, v196, v202, 0
	v_cvt_scalef32_pk_f16_fp4 v195, v67, 1.0 op_sel:[1,0,0]
	v_pk_fma_f16 v181, v197, v202, 0
	v_cvt_scalef32_pk_f16_fp4 v196, v67, 1.0 op_sel:[0,1,0]
	v_pk_fma_f16 v182, v194, v202, 0
	v_cvt_scalef32_pk_f16_fp4 v197, v67, 1.0 op_sel:[1,1,0]
	v_pk_fma_f16 v183, v195, v202, 0
	v_cvt_scalef32_pk_f16_fp4 v194, v68, 1.0
	v_pk_fma_f16 v184, v196, v202, 0
	v_cvt_scalef32_pk_f16_fp4 v195, v68, 1.0 op_sel:[1,0,0]
	v_pk_fma_f16 v185, v197, v202, 0
	v_cvt_scalef32_pk_f16_fp4 v196, v68, 1.0 op_sel:[0,1,0]
	v_pk_fma_f16 v186, v194, v202, 0
	v_cvt_scalef32_pk_f16_fp4 v197, v68, 1.0 op_sel:[1,1,0]
	v_pk_fma_f16 v187, v195, v202, 0
	v_cvt_scalef32_pk_f16_fp4 v194, v69, 1.0
	v_pk_fma_f16 v188, v196, v202, 0
	v_cvt_scalef32_pk_f16_fp4 v195, v69, 1.0 op_sel:[1,0,0]
	v_pk_fma_f16 v189, v197, v202, 0
	v_cvt_scalef32_pk_f16_fp4 v196, v69, 1.0 op_sel:[0,1,0]
	v_pk_fma_f16 v190, v194, v202, 0
	v_cvt_scalef32_pk_f16_fp4 v197, v69, 1.0 op_sel:[1,1,0]
	v_pk_fma_f16 v191, v195, v202, 0
	v_pk_fma_f16 v192, v196, v202, 0
	v_pk_fma_f16 v193, v197, v202, 0
	v_mul_u32_u24_sdwa v203, v138, s93 dst_sel:DWORD dst_unused:UNUSED_PAD src0_sel:WORD_1 src1_sel:DWORD
	v_cvt_scalef32_pk_f16_fp4 v194, v70, 1.0
	v_cvt_scalef32_pk_f16_fp4 v195, v70, 1.0 op_sel:[1,0,0]
	v_cvt_scalef32_pk_f16_fp4 v196, v70, 1.0 op_sel:[0,1,0]
	v_pk_fma_f16 v178, v194, v203, v178
	v_cvt_scalef32_pk_f16_fp4 v197, v70, 1.0 op_sel:[1,1,0]
	v_pk_fma_f16 v179, v195, v203, v179
	v_cvt_scalef32_pk_f16_fp4 v194, v71, 1.0
	v_pk_fma_f16 v180, v196, v203, v180
	v_cvt_scalef32_pk_f16_fp4 v195, v71, 1.0 op_sel:[1,0,0]
	v_pk_fma_f16 v181, v197, v203, v181
	v_cvt_scalef32_pk_f16_fp4 v196, v71, 1.0 op_sel:[0,1,0]
	v_pk_fma_f16 v182, v194, v203, v182
	v_cvt_scalef32_pk_f16_fp4 v197, v71, 1.0 op_sel:[1,1,0]
	v_pk_fma_f16 v183, v195, v203, v183
	v_cvt_scalef32_pk_f16_fp4 v194, v72, 1.0
	v_pk_fma_f16 v184, v196, v203, v184
	v_cvt_scalef32_pk_f16_fp4 v195, v72, 1.0 op_sel:[1,0,0]
	v_pk_fma_f16 v185, v197, v203, v185
	v_cvt_scalef32_pk_f16_fp4 v196, v72, 1.0 op_sel:[0,1,0]
	v_pk_fma_f16 v186, v194, v203, v186
	v_cvt_scalef32_pk_f16_fp4 v197, v72, 1.0 op_sel:[1,1,0]
	v_pk_fma_f16 v187, v195, v203, v187
	v_cvt_scalef32_pk_f16_fp4 v194, v73, 1.0
	v_pk_fma_f16 v188, v196, v203, v188
	v_cvt_scalef32_pk_f16_fp4 v195, v73, 1.0 op_sel:[1,0,0]
	v_pk_fma_f16 v189, v197, v203, v189
	v_cvt_scalef32_pk_f16_fp4 v196, v73, 1.0 op_sel:[0,1,0]
	v_pk_fma_f16 v190, v194, v203, v190
	v_cvt_scalef32_pk_f16_fp4 v197, v73, 1.0 op_sel:[1,1,0]
	v_pk_fma_f16 v191, v195, v203, v191
	v_pk_fma_f16 v192, v196, v203, v192
	v_pk_fma_f16 v193, v197, v203, v193
	v_mul_u32_u24_sdwa v202, v139, s93 dst_sel:DWORD dst_unused:UNUSED_PAD src0_sel:WORD_0 src1_sel:DWORD
	v_cvt_scalef32_pk_f16_fp4 v194, v74, 1.0
	v_cvt_scalef32_pk_f16_fp4 v195, v74, 1.0 op_sel:[1,0,0]
	v_cvt_scalef32_pk_f16_fp4 v196, v74, 1.0 op_sel:[0,1,0]
	v_pk_fma_f16 v178, v194, v202, v178
	v_cvt_scalef32_pk_f16_fp4 v197, v74, 1.0 op_sel:[1,1,0]
	v_pk_fma_f16 v179, v195, v202, v179
	v_cvt_scalef32_pk_f16_fp4 v194, v75, 1.0
	v_pk_fma_f16 v180, v196, v202, v180
	v_cvt_scalef32_pk_f16_fp4 v195, v75, 1.0 op_sel:[1,0,0]
	v_pk_fma_f16 v181, v197, v202, v181
	v_cvt_scalef32_pk_f16_fp4 v196, v75, 1.0 op_sel:[0,1,0]
	v_pk_fma_f16 v182, v194, v202, v182
	v_cvt_scalef32_pk_f16_fp4 v197, v75, 1.0 op_sel:[1,1,0]
	v_pk_fma_f16 v183, v195, v202, v183
	v_cvt_scalef32_pk_f16_fp4 v194, v76, 1.0
	v_pk_fma_f16 v184, v196, v202, v184
	v_cvt_scalef32_pk_f16_fp4 v195, v76, 1.0 op_sel:[1,0,0]
	v_pk_fma_f16 v185, v197, v202, v185
	v_cvt_scalef32_pk_f16_fp4 v196, v76, 1.0 op_sel:[0,1,0]
	v_pk_fma_f16 v186, v194, v202, v186
	v_cvt_scalef32_pk_f16_fp4 v197, v76, 1.0 op_sel:[1,1,0]
	v_pk_fma_f16 v187, v195, v202, v187
	v_cvt_scalef32_pk_f16_fp4 v194, v77, 1.0
	v_pk_fma_f16 v188, v196, v202, v188
	v_cvt_scalef32_pk_f16_fp4 v195, v77, 1.0 op_sel:[1,0,0]
	v_pk_fma_f16 v189, v197, v202, v189
	v_cvt_scalef32_pk_f16_fp4 v196, v77, 1.0 op_sel:[0,1,0]
	v_pk_fma_f16 v190, v194, v202, v190
	v_cvt_scalef32_pk_f16_fp4 v197, v77, 1.0 op_sel:[1,1,0]
	v_pk_fma_f16 v191, v195, v202, v191
	v_pk_fma_f16 v192, v196, v202, v192
	v_pk_fma_f16 v193, v197, v202, v193
	v_mul_u32_u24_sdwa v203, v139, s93 dst_sel:DWORD dst_unused:UNUSED_PAD src0_sel:WORD_1 src1_sel:DWORD
	v_cvt_scalef32_pk_f16_fp4 v194, v78, 1.0
	v_cvt_scalef32_pk_f16_fp4 v195, v78, 1.0 op_sel:[1,0,0]
	v_cvt_scalef32_pk_f16_fp4 v196, v78, 1.0 op_sel:[0,1,0]
	v_pk_fma_f16 v178, v194, v203, v178
	v_cvt_scalef32_pk_f16_fp4 v197, v78, 1.0 op_sel:[1,1,0]
	v_pk_fma_f16 v179, v195, v203, v179
	v_cvt_scalef32_pk_f16_fp4 v194, v79, 1.0
	v_pk_fma_f16 v180, v196, v203, v180
	v_cvt_scalef32_pk_f16_fp4 v195, v79, 1.0 op_sel:[1,0,0]
	v_pk_fma_f16 v181, v197, v203, v181
	v_cvt_scalef32_pk_f16_fp4 v196, v79, 1.0 op_sel:[0,1,0]
	v_pk_fma_f16 v182, v194, v203, v182
	v_cvt_scalef32_pk_f16_fp4 v197, v79, 1.0 op_sel:[1,1,0]
	v_pk_fma_f16 v183, v195, v203, v183
	v_cvt_scalef32_pk_f16_fp4 v194, v80, 1.0
	v_pk_fma_f16 v184, v196, v203, v184
	v_cvt_scalef32_pk_f16_fp4 v195, v80, 1.0 op_sel:[1,0,0]
	v_pk_fma_f16 v185, v197, v203, v185
	v_cvt_scalef32_pk_f16_fp4 v196, v80, 1.0 op_sel:[0,1,0]
	v_pk_fma_f16 v186, v194, v203, v186
	v_cvt_scalef32_pk_f16_fp4 v197, v80, 1.0 op_sel:[1,1,0]
	v_pk_fma_f16 v187, v195, v203, v187
	v_cvt_scalef32_pk_f16_fp4 v194, v81, 1.0
	v_pk_fma_f16 v188, v196, v203, v188
	v_cvt_scalef32_pk_f16_fp4 v195, v81, 1.0 op_sel:[1,0,0]
	v_pk_fma_f16 v189, v197, v203, v189
	v_cvt_scalef32_pk_f16_fp4 v196, v81, 1.0 op_sel:[0,1,0]
	v_pk_fma_f16 v190, v194, v203, v190
	v_cvt_scalef32_pk_f16_fp4 v197, v81, 1.0 op_sel:[1,1,0]
	v_pk_fma_f16 v191, v195, v203, v191
	v_pk_fma_f16 v192, v196, v203, v192
	v_pk_fma_f16 v193, v197, v203, v193
	v_mul_u32_u24_sdwa v202, v140, s93 dst_sel:DWORD dst_unused:UNUSED_PAD src0_sel:WORD_0 src1_sel:DWORD
	v_cvt_scalef32_pk_f16_fp4 v194, v82, 1.0
	v_cvt_scalef32_pk_f16_fp4 v195, v82, 1.0 op_sel:[1,0,0]
	v_cvt_scalef32_pk_f16_fp4 v196, v82, 1.0 op_sel:[0,1,0]
	v_pk_fma_f16 v178, v194, v202, v178
	v_cvt_scalef32_pk_f16_fp4 v197, v82, 1.0 op_sel:[1,1,0]
	v_pk_fma_f16 v179, v195, v202, v179
	v_cvt_scalef32_pk_f16_fp4 v194, v83, 1.0
	v_pk_fma_f16 v180, v196, v202, v180
	v_cvt_scalef32_pk_f16_fp4 v195, v83, 1.0 op_sel:[1,0,0]
	v_pk_fma_f16 v181, v197, v202, v181
	v_cvt_scalef32_pk_f16_fp4 v196, v83, 1.0 op_sel:[0,1,0]
	v_pk_fma_f16 v182, v194, v202, v182
	v_cvt_scalef32_pk_f16_fp4 v197, v83, 1.0 op_sel:[1,1,0]
	v_pk_fma_f16 v183, v195, v202, v183
	v_cvt_scalef32_pk_f16_fp4 v194, v84, 1.0
	v_pk_fma_f16 v184, v196, v202, v184
	v_cvt_scalef32_pk_f16_fp4 v195, v84, 1.0 op_sel:[1,0,0]
	v_pk_fma_f16 v185, v197, v202, v185
	v_cvt_scalef32_pk_f16_fp4 v196, v84, 1.0 op_sel:[0,1,0]
	v_pk_fma_f16 v186, v194, v202, v186
	v_cvt_scalef32_pk_f16_fp4 v197, v84, 1.0 op_sel:[1,1,0]
	v_pk_fma_f16 v187, v195, v202, v187
	v_cvt_scalef32_pk_f16_fp4 v194, v85, 1.0
	v_pk_fma_f16 v188, v196, v202, v188
	v_cvt_scalef32_pk_f16_fp4 v195, v85, 1.0 op_sel:[1,0,0]
	v_pk_fma_f16 v189, v197, v202, v189
	v_cvt_scalef32_pk_f16_fp4 v196, v85, 1.0 op_sel:[0,1,0]
	v_pk_fma_f16 v190, v194, v202, v190
	v_cvt_scalef32_pk_f16_fp4 v197, v85, 1.0 op_sel:[1,1,0]
	v_pk_fma_f16 v191, v195, v202, v191
	v_pk_fma_f16 v192, v196, v202, v192
	v_pk_fma_f16 v193, v197, v202, v193
	v_mul_u32_u24_sdwa v203, v140, s93 dst_sel:DWORD dst_unused:UNUSED_PAD src0_sel:WORD_1 src1_sel:DWORD
	v_cvt_scalef32_pk_f16_fp4 v194, v86, 1.0
	v_cvt_scalef32_pk_f16_fp4 v195, v86, 1.0 op_sel:[1,0,0]
	v_cvt_scalef32_pk_f16_fp4 v196, v86, 1.0 op_sel:[0,1,0]
	v_pk_fma_f16 v178, v194, v203, v178
	v_cvt_scalef32_pk_f16_fp4 v197, v86, 1.0 op_sel:[1,1,0]
	v_pk_fma_f16 v179, v195, v203, v179
	v_cvt_scalef32_pk_f16_fp4 v194, v87, 1.0
	v_pk_fma_f16 v180, v196, v203, v180
	v_cvt_scalef32_pk_f16_fp4 v195, v87, 1.0 op_sel:[1,0,0]
	v_pk_fma_f16 v181, v197, v203, v181
	v_cvt_scalef32_pk_f16_fp4 v196, v87, 1.0 op_sel:[0,1,0]
	v_pk_fma_f16 v182, v194, v203, v182
	v_cvt_scalef32_pk_f16_fp4 v197, v87, 1.0 op_sel:[1,1,0]
	v_pk_fma_f16 v183, v195, v203, v183
	v_cvt_scalef32_pk_f16_fp4 v194, v88, 1.0
	v_pk_fma_f16 v184, v196, v203, v184
	v_cvt_scalef32_pk_f16_fp4 v195, v88, 1.0 op_sel:[1,0,0]
	v_pk_fma_f16 v185, v197, v203, v185
	v_cvt_scalef32_pk_f16_fp4 v196, v88, 1.0 op_sel:[0,1,0]
	v_pk_fma_f16 v186, v194, v203, v186
	v_cvt_scalef32_pk_f16_fp4 v197, v88, 1.0 op_sel:[1,1,0]
	v_pk_fma_f16 v187, v195, v203, v187
	v_cvt_scalef32_pk_f16_fp4 v194, v89, 1.0
	v_pk_fma_f16 v188, v196, v203, v188
	v_cvt_scalef32_pk_f16_fp4 v195, v89, 1.0 op_sel:[1,0,0]
	v_pk_fma_f16 v189, v197, v203, v189
	v_cvt_scalef32_pk_f16_fp4 v196, v89, 1.0 op_sel:[0,1,0]
	v_pk_fma_f16 v190, v194, v203, v190
	v_cvt_scalef32_pk_f16_fp4 v197, v89, 1.0 op_sel:[1,1,0]
	v_pk_fma_f16 v191, v195, v203, v191
	v_pk_fma_f16 v192, v196, v203, v192
	v_pk_fma_f16 v193, v197, v203, v193
	v_mul_u32_u24_sdwa v202, v141, s93 dst_sel:DWORD dst_unused:UNUSED_PAD src0_sel:WORD_0 src1_sel:DWORD
	v_cvt_scalef32_pk_f16_fp4 v194, v90, 1.0
	v_cvt_scalef32_pk_f16_fp4 v195, v90, 1.0 op_sel:[1,0,0]
	v_cvt_scalef32_pk_f16_fp4 v196, v90, 1.0 op_sel:[0,1,0]
	v_pk_fma_f16 v178, v194, v202, v178
	v_cvt_scalef32_pk_f16_fp4 v197, v90, 1.0 op_sel:[1,1,0]
	v_pk_fma_f16 v179, v195, v202, v179
	v_cvt_scalef32_pk_f16_fp4 v194, v91, 1.0
	v_pk_fma_f16 v180, v196, v202, v180
	v_cvt_scalef32_pk_f16_fp4 v195, v91, 1.0 op_sel:[1,0,0]
	v_pk_fma_f16 v181, v197, v202, v181
	v_cvt_scalef32_pk_f16_fp4 v196, v91, 1.0 op_sel:[0,1,0]
	v_pk_fma_f16 v182, v194, v202, v182
	v_cvt_scalef32_pk_f16_fp4 v197, v91, 1.0 op_sel:[1,1,0]
	v_pk_fma_f16 v183, v195, v202, v183
	v_cvt_scalef32_pk_f16_fp4 v194, v92, 1.0
	v_pk_fma_f16 v184, v196, v202, v184
	v_cvt_scalef32_pk_f16_fp4 v195, v92, 1.0 op_sel:[1,0,0]
	v_pk_fma_f16 v185, v197, v202, v185
	v_cvt_scalef32_pk_f16_fp4 v196, v92, 1.0 op_sel:[0,1,0]
	v_pk_fma_f16 v186, v194, v202, v186
	v_cvt_scalef32_pk_f16_fp4 v197, v92, 1.0 op_sel:[1,1,0]
	v_pk_fma_f16 v187, v195, v202, v187
	v_cvt_scalef32_pk_f16_fp4 v194, v93, 1.0
	v_pk_fma_f16 v188, v196, v202, v188
	v_cvt_scalef32_pk_f16_fp4 v195, v93, 1.0 op_sel:[1,0,0]
	v_pk_fma_f16 v189, v197, v202, v189
	v_cvt_scalef32_pk_f16_fp4 v196, v93, 1.0 op_sel:[0,1,0]
	v_pk_fma_f16 v190, v194, v202, v190
	v_cvt_scalef32_pk_f16_fp4 v197, v93, 1.0 op_sel:[1,1,0]
	v_pk_fma_f16 v191, v195, v202, v191
	v_pk_fma_f16 v192, v196, v202, v192
	v_pk_fma_f16 v193, v197, v202, v193
	v_mul_u32_u24_sdwa v203, v141, s93 dst_sel:DWORD dst_unused:UNUSED_PAD src0_sel:WORD_1 src1_sel:DWORD
	v_cvt_scalef32_pk_f16_fp4 v194, v94, 1.0
	v_cvt_scalef32_pk_f16_fp4 v195, v94, 1.0 op_sel:[1,0,0]
	v_cvt_scalef32_pk_f16_fp4 v196, v94, 1.0 op_sel:[0,1,0]
	v_pk_fma_f16 v178, v194, v203, v178
	v_cvt_scalef32_pk_f16_fp4 v197, v94, 1.0 op_sel:[1,1,0]
	v_pk_fma_f16 v179, v195, v203, v179
	v_cvt_scalef32_pk_f16_fp4 v194, v95, 1.0
	v_pk_fma_f16 v180, v196, v203, v180
	v_cvt_scalef32_pk_f16_fp4 v195, v95, 1.0 op_sel:[1,0,0]
	v_pk_fma_f16 v181, v197, v203, v181
	v_cvt_scalef32_pk_f16_fp4 v196, v95, 1.0 op_sel:[0,1,0]
	v_pk_fma_f16 v182, v194, v203, v182
	v_cvt_scalef32_pk_f16_fp4 v197, v95, 1.0 op_sel:[1,1,0]
	v_pk_fma_f16 v183, v195, v203, v183
	v_cvt_scalef32_pk_f16_fp4 v194, v96, 1.0
	v_pk_fma_f16 v184, v196, v203, v184
	v_cvt_scalef32_pk_f16_fp4 v195, v96, 1.0 op_sel:[1,0,0]
	v_pk_fma_f16 v185, v197, v203, v185
	v_cvt_scalef32_pk_f16_fp4 v196, v96, 1.0 op_sel:[0,1,0]
	v_pk_fma_f16 v186, v194, v203, v186
	v_cvt_scalef32_pk_f16_fp4 v197, v96, 1.0 op_sel:[1,1,0]
	v_pk_fma_f16 v187, v195, v203, v187
	v_cvt_scalef32_pk_f16_fp4 v194, v97, 1.0
	v_pk_fma_f16 v188, v196, v203, v188
	v_cvt_scalef32_pk_f16_fp4 v195, v97, 1.0 op_sel:[1,0,0]
	v_pk_fma_f16 v189, v197, v203, v189
	v_cvt_scalef32_pk_f16_fp4 v196, v97, 1.0 op_sel:[0,1,0]
	v_pk_fma_f16 v190, v194, v203, v190
	v_cvt_scalef32_pk_f16_fp4 v197, v97, 1.0 op_sel:[1,1,0]
	v_pk_fma_f16 v191, v195, v203, v191
	v_pk_fma_f16 v192, v196, v203, v192
	v_pk_fma_f16 v193, v197, v203, v193
	v_mul_u32_u24_sdwa v202, v142, s93 dst_sel:DWORD dst_unused:UNUSED_PAD src0_sel:WORD_0 src1_sel:DWORD
	v_cvt_scalef32_pk_f16_fp4 v194, v98, 1.0
	v_cvt_scalef32_pk_f16_fp4 v195, v98, 1.0 op_sel:[1,0,0]
	v_cvt_scalef32_pk_f16_fp4 v196, v98, 1.0 op_sel:[0,1,0]
	v_pk_fma_f16 v178, v194, v202, v178
	v_cvt_scalef32_pk_f16_fp4 v197, v98, 1.0 op_sel:[1,1,0]
	v_pk_fma_f16 v179, v195, v202, v179
	v_cvt_scalef32_pk_f16_fp4 v194, v99, 1.0
	v_pk_fma_f16 v180, v196, v202, v180
	v_cvt_scalef32_pk_f16_fp4 v195, v99, 1.0 op_sel:[1,0,0]
	v_pk_fma_f16 v181, v197, v202, v181
	v_cvt_scalef32_pk_f16_fp4 v196, v99, 1.0 op_sel:[0,1,0]
	v_pk_fma_f16 v182, v194, v202, v182
	v_cvt_scalef32_pk_f16_fp4 v197, v99, 1.0 op_sel:[1,1,0]
	v_pk_fma_f16 v183, v195, v202, v183
	v_cvt_scalef32_pk_f16_fp4 v194, v100, 1.0
	v_pk_fma_f16 v184, v196, v202, v184
	v_cvt_scalef32_pk_f16_fp4 v195, v100, 1.0 op_sel:[1,0,0]
	v_pk_fma_f16 v185, v197, v202, v185
	v_cvt_scalef32_pk_f16_fp4 v196, v100, 1.0 op_sel:[0,1,0]
	v_pk_fma_f16 v186, v194, v202, v186
	v_cvt_scalef32_pk_f16_fp4 v197, v100, 1.0 op_sel:[1,1,0]
	v_pk_fma_f16 v187, v195, v202, v187
	v_cvt_scalef32_pk_f16_fp4 v194, v101, 1.0
	v_pk_fma_f16 v188, v196, v202, v188
	v_cvt_scalef32_pk_f16_fp4 v195, v101, 1.0 op_sel:[1,0,0]
	v_pk_fma_f16 v189, v197, v202, v189
	v_cvt_scalef32_pk_f16_fp4 v196, v101, 1.0 op_sel:[0,1,0]
	v_pk_fma_f16 v190, v194, v202, v190
	v_cvt_scalef32_pk_f16_fp4 v197, v101, 1.0 op_sel:[1,1,0]
	v_pk_fma_f16 v191, v195, v202, v191
	v_pk_fma_f16 v192, v196, v202, v192
	v_pk_fma_f16 v193, v197, v202, v193
	v_mul_u32_u24_sdwa v203, v142, s93 dst_sel:DWORD dst_unused:UNUSED_PAD src0_sel:WORD_1 src1_sel:DWORD
	v_cvt_scalef32_pk_f16_fp4 v194, v102, 1.0
	v_cvt_scalef32_pk_f16_fp4 v195, v102, 1.0 op_sel:[1,0,0]
	v_cvt_scalef32_pk_f16_fp4 v196, v102, 1.0 op_sel:[0,1,0]
	v_pk_fma_f16 v178, v194, v203, v178
	v_cvt_scalef32_pk_f16_fp4 v197, v102, 1.0 op_sel:[1,1,0]
	v_pk_fma_f16 v179, v195, v203, v179
	v_cvt_scalef32_pk_f16_fp4 v194, v103, 1.0
	v_pk_fma_f16 v180, v196, v203, v180
	v_cvt_scalef32_pk_f16_fp4 v195, v103, 1.0 op_sel:[1,0,0]
	v_pk_fma_f16 v181, v197, v203, v181
	v_cvt_scalef32_pk_f16_fp4 v196, v103, 1.0 op_sel:[0,1,0]
	v_pk_fma_f16 v182, v194, v203, v182
	v_cvt_scalef32_pk_f16_fp4 v197, v103, 1.0 op_sel:[1,1,0]
	v_pk_fma_f16 v183, v195, v203, v183
	v_cvt_scalef32_pk_f16_fp4 v194, v104, 1.0
	v_pk_fma_f16 v184, v196, v203, v184
	v_cvt_scalef32_pk_f16_fp4 v195, v104, 1.0 op_sel:[1,0,0]
	v_pk_fma_f16 v185, v197, v203, v185
	v_cvt_scalef32_pk_f16_fp4 v196, v104, 1.0 op_sel:[0,1,0]
	v_pk_fma_f16 v186, v194, v203, v186
	v_cvt_scalef32_pk_f16_fp4 v197, v104, 1.0 op_sel:[1,1,0]
	v_pk_fma_f16 v187, v195, v203, v187
	v_cvt_scalef32_pk_f16_fp4 v194, v105, 1.0
	v_pk_fma_f16 v188, v196, v203, v188
	v_cvt_scalef32_pk_f16_fp4 v195, v105, 1.0 op_sel:[1,0,0]
	v_pk_fma_f16 v189, v197, v203, v189
	v_cvt_scalef32_pk_f16_fp4 v196, v105, 1.0 op_sel:[0,1,0]
	v_pk_fma_f16 v190, v194, v203, v190
	v_cvt_scalef32_pk_f16_fp4 v197, v105, 1.0 op_sel:[1,1,0]
	v_pk_fma_f16 v191, v195, v203, v191
	v_pk_fma_f16 v192, v196, v203, v192
	v_pk_fma_f16 v193, v197, v203, v193
	v_mul_u32_u24_sdwa v202, v143, s93 dst_sel:DWORD dst_unused:UNUSED_PAD src0_sel:WORD_0 src1_sel:DWORD
	v_cvt_scalef32_pk_f16_fp4 v194, v106, 1.0
	v_cvt_scalef32_pk_f16_fp4 v195, v106, 1.0 op_sel:[1,0,0]
	v_cvt_scalef32_pk_f16_fp4 v196, v106, 1.0 op_sel:[0,1,0]
	v_pk_fma_f16 v178, v194, v202, v178
	v_cvt_scalef32_pk_f16_fp4 v197, v106, 1.0 op_sel:[1,1,0]
	v_pk_fma_f16 v179, v195, v202, v179
	v_cvt_scalef32_pk_f16_fp4 v194, v107, 1.0
	v_pk_fma_f16 v180, v196, v202, v180
	v_cvt_scalef32_pk_f16_fp4 v195, v107, 1.0 op_sel:[1,0,0]
	v_pk_fma_f16 v181, v197, v202, v181
	v_cvt_scalef32_pk_f16_fp4 v196, v107, 1.0 op_sel:[0,1,0]
	v_pk_fma_f16 v182, v194, v202, v182
	v_cvt_scalef32_pk_f16_fp4 v197, v107, 1.0 op_sel:[1,1,0]
	v_pk_fma_f16 v183, v195, v202, v183
	v_cvt_scalef32_pk_f16_fp4 v194, v108, 1.0
	v_pk_fma_f16 v184, v196, v202, v184
	v_cvt_scalef32_pk_f16_fp4 v195, v108, 1.0 op_sel:[1,0,0]
	v_pk_fma_f16 v185, v197, v202, v185
	v_cvt_scalef32_pk_f16_fp4 v196, v108, 1.0 op_sel:[0,1,0]
	v_pk_fma_f16 v186, v194, v202, v186
	v_cvt_scalef32_pk_f16_fp4 v197, v108, 1.0 op_sel:[1,1,0]
	v_pk_fma_f16 v187, v195, v202, v187
	v_cvt_scalef32_pk_f16_fp4 v194, v109, 1.0
	v_pk_fma_f16 v188, v196, v202, v188
	v_cvt_scalef32_pk_f16_fp4 v195, v109, 1.0 op_sel:[1,0,0]
	v_pk_fma_f16 v189, v197, v202, v189
	v_cvt_scalef32_pk_f16_fp4 v196, v109, 1.0 op_sel:[0,1,0]
	v_pk_fma_f16 v190, v194, v202, v190
	v_cvt_scalef32_pk_f16_fp4 v197, v109, 1.0 op_sel:[1,1,0]
	v_pk_fma_f16 v191, v195, v202, v191
	v_pk_fma_f16 v192, v196, v202, v192
	v_pk_fma_f16 v193, v197, v202, v193
	v_mul_u32_u24_sdwa v203, v143, s93 dst_sel:DWORD dst_unused:UNUSED_PAD src0_sel:WORD_1 src1_sel:DWORD
	v_cvt_scalef32_pk_f16_fp4 v194, v110, 1.0
	v_cvt_scalef32_pk_f16_fp4 v195, v110, 1.0 op_sel:[1,0,0]
	v_cvt_scalef32_pk_f16_fp4 v196, v110, 1.0 op_sel:[0,1,0]
	v_pk_fma_f16 v178, v194, v203, v178
	v_cvt_scalef32_pk_f16_fp4 v197, v110, 1.0 op_sel:[1,1,0]
	v_pk_fma_f16 v179, v195, v203, v179
	v_cvt_scalef32_pk_f16_fp4 v194, v111, 1.0
	v_pk_fma_f16 v180, v196, v203, v180
	v_cvt_scalef32_pk_f16_fp4 v195, v111, 1.0 op_sel:[1,0,0]
	v_pk_fma_f16 v181, v197, v203, v181
	v_cvt_scalef32_pk_f16_fp4 v196, v111, 1.0 op_sel:[0,1,0]
	v_pk_fma_f16 v182, v194, v203, v182
	v_cvt_scalef32_pk_f16_fp4 v197, v111, 1.0 op_sel:[1,1,0]
	v_pk_fma_f16 v183, v195, v203, v183
	v_cvt_scalef32_pk_f16_fp4 v194, v112, 1.0
	v_pk_fma_f16 v184, v196, v203, v184
	v_cvt_scalef32_pk_f16_fp4 v195, v112, 1.0 op_sel:[1,0,0]
	v_pk_fma_f16 v185, v197, v203, v185
	v_cvt_scalef32_pk_f16_fp4 v196, v112, 1.0 op_sel:[0,1,0]
	v_pk_fma_f16 v186, v194, v203, v186
	v_cvt_scalef32_pk_f16_fp4 v197, v112, 1.0 op_sel:[1,1,0]
	v_pk_fma_f16 v187, v195, v203, v187
	v_cvt_scalef32_pk_f16_fp4 v194, v113, 1.0
	v_pk_fma_f16 v188, v196, v203, v188
	v_cvt_scalef32_pk_f16_fp4 v195, v113, 1.0 op_sel:[1,0,0]
	v_pk_fma_f16 v189, v197, v203, v189
	v_cvt_scalef32_pk_f16_fp4 v196, v113, 1.0 op_sel:[0,1,0]
	v_pk_fma_f16 v190, v194, v203, v190
	v_cvt_scalef32_pk_f16_fp4 v197, v113, 1.0 op_sel:[1,1,0]
	v_pk_fma_f16 v191, v195, v203, v191
	v_pk_fma_f16 v192, v196, v203, v192
	v_pk_fma_f16 v193, v197, v203, v193
	v_mul_u32_u24_sdwa v202, v144, s93 dst_sel:DWORD dst_unused:UNUSED_PAD src0_sel:WORD_0 src1_sel:DWORD
	v_cvt_scalef32_pk_f16_fp4 v194, v114, 1.0
	v_cvt_scalef32_pk_f16_fp4 v195, v114, 1.0 op_sel:[1,0,0]
	v_cvt_scalef32_pk_f16_fp4 v196, v114, 1.0 op_sel:[0,1,0]
	v_pk_fma_f16 v178, v194, v202, v178
	v_cvt_scalef32_pk_f16_fp4 v197, v114, 1.0 op_sel:[1,1,0]
	v_pk_fma_f16 v179, v195, v202, v179
	v_cvt_scalef32_pk_f16_fp4 v194, v115, 1.0
	v_pk_fma_f16 v180, v196, v202, v180
	v_cvt_scalef32_pk_f16_fp4 v195, v115, 1.0 op_sel:[1,0,0]
	v_pk_fma_f16 v181, v197, v202, v181
	v_cvt_scalef32_pk_f16_fp4 v196, v115, 1.0 op_sel:[0,1,0]
	v_pk_fma_f16 v182, v194, v202, v182
	v_cvt_scalef32_pk_f16_fp4 v197, v115, 1.0 op_sel:[1,1,0]
	v_pk_fma_f16 v183, v195, v202, v183
	v_cvt_scalef32_pk_f16_fp4 v194, v116, 1.0
	v_pk_fma_f16 v184, v196, v202, v184
	v_cvt_scalef32_pk_f16_fp4 v195, v116, 1.0 op_sel:[1,0,0]
	v_pk_fma_f16 v185, v197, v202, v185
	v_cvt_scalef32_pk_f16_fp4 v196, v116, 1.0 op_sel:[0,1,0]
	v_pk_fma_f16 v186, v194, v202, v186
	v_cvt_scalef32_pk_f16_fp4 v197, v116, 1.0 op_sel:[1,1,0]
	v_pk_fma_f16 v187, v195, v202, v187
	v_cvt_scalef32_pk_f16_fp4 v194, v117, 1.0
	v_pk_fma_f16 v188, v196, v202, v188
	v_cvt_scalef32_pk_f16_fp4 v195, v117, 1.0 op_sel:[1,0,0]
	v_pk_fma_f16 v189, v197, v202, v189
	v_cvt_scalef32_pk_f16_fp4 v196, v117, 1.0 op_sel:[0,1,0]
	v_pk_fma_f16 v190, v194, v202, v190
	v_cvt_scalef32_pk_f16_fp4 v197, v117, 1.0 op_sel:[1,1,0]
	v_pk_fma_f16 v191, v195, v202, v191
	v_pk_fma_f16 v192, v196, v202, v192
	v_pk_fma_f16 v193, v197, v202, v193
	v_mul_u32_u24_sdwa v203, v144, s93 dst_sel:DWORD dst_unused:UNUSED_PAD src0_sel:WORD_1 src1_sel:DWORD
	v_cvt_scalef32_pk_f16_fp4 v194, v118, 1.0
	v_cvt_scalef32_pk_f16_fp4 v195, v118, 1.0 op_sel:[1,0,0]
	v_cvt_scalef32_pk_f16_fp4 v196, v118, 1.0 op_sel:[0,1,0]
	v_pk_fma_f16 v178, v194, v203, v178
	v_cvt_scalef32_pk_f16_fp4 v197, v118, 1.0 op_sel:[1,1,0]
	v_pk_fma_f16 v179, v195, v203, v179
	v_cvt_scalef32_pk_f16_fp4 v194, v119, 1.0
	v_pk_fma_f16 v180, v196, v203, v180
	v_cvt_scalef32_pk_f16_fp4 v195, v119, 1.0 op_sel:[1,0,0]
	v_pk_fma_f16 v181, v197, v203, v181
	v_cvt_scalef32_pk_f16_fp4 v196, v119, 1.0 op_sel:[0,1,0]
	v_pk_fma_f16 v182, v194, v203, v182
	v_cvt_scalef32_pk_f16_fp4 v197, v119, 1.0 op_sel:[1,1,0]
	v_pk_fma_f16 v183, v195, v203, v183
	v_cvt_scalef32_pk_f16_fp4 v194, v120, 1.0
	v_pk_fma_f16 v184, v196, v203, v184
	v_cvt_scalef32_pk_f16_fp4 v195, v120, 1.0 op_sel:[1,0,0]
	v_pk_fma_f16 v185, v197, v203, v185
	v_cvt_scalef32_pk_f16_fp4 v196, v120, 1.0 op_sel:[0,1,0]
	v_pk_fma_f16 v186, v194, v203, v186
	v_cvt_scalef32_pk_f16_fp4 v197, v120, 1.0 op_sel:[1,1,0]
	v_pk_fma_f16 v187, v195, v203, v187
	v_cvt_scalef32_pk_f16_fp4 v194, v121, 1.0
	v_pk_fma_f16 v188, v196, v203, v188
	v_cvt_scalef32_pk_f16_fp4 v195, v121, 1.0 op_sel:[1,0,0]
	v_pk_fma_f16 v189, v197, v203, v189
	v_cvt_scalef32_pk_f16_fp4 v196, v121, 1.0 op_sel:[0,1,0]
	v_pk_fma_f16 v190, v194, v203, v190
	v_cvt_scalef32_pk_f16_fp4 v197, v121, 1.0 op_sel:[1,1,0]
	v_pk_fma_f16 v191, v195, v203, v191
	v_pk_fma_f16 v192, v196, v203, v192
	v_pk_fma_f16 v193, v197, v203, v193
	v_mul_u32_u24_sdwa v202, v145, s93 dst_sel:DWORD dst_unused:UNUSED_PAD src0_sel:WORD_0 src1_sel:DWORD
	v_cvt_scalef32_pk_f16_fp4 v194, v122, 1.0
	v_cvt_scalef32_pk_f16_fp4 v195, v122, 1.0 op_sel:[1,0,0]
	v_cvt_scalef32_pk_f16_fp4 v196, v122, 1.0 op_sel:[0,1,0]
	v_pk_fma_f16 v178, v194, v202, v178
	v_cvt_scalef32_pk_f16_fp4 v197, v122, 1.0 op_sel:[1,1,0]
	v_pk_fma_f16 v179, v195, v202, v179
	v_cvt_scalef32_pk_f16_fp4 v194, v123, 1.0
	v_pk_fma_f16 v180, v196, v202, v180
	v_cvt_scalef32_pk_f16_fp4 v195, v123, 1.0 op_sel:[1,0,0]
	v_pk_fma_f16 v181, v197, v202, v181
	v_cvt_scalef32_pk_f16_fp4 v196, v123, 1.0 op_sel:[0,1,0]
	v_pk_fma_f16 v182, v194, v202, v182
	v_cvt_scalef32_pk_f16_fp4 v197, v123, 1.0 op_sel:[1,1,0]
	v_pk_fma_f16 v183, v195, v202, v183
	v_cvt_scalef32_pk_f16_fp4 v194, v124, 1.0
	v_pk_fma_f16 v184, v196, v202, v184
	v_cvt_scalef32_pk_f16_fp4 v195, v124, 1.0 op_sel:[1,0,0]
	v_pk_fma_f16 v185, v197, v202, v185
	v_cvt_scalef32_pk_f16_fp4 v196, v124, 1.0 op_sel:[0,1,0]
	v_pk_fma_f16 v186, v194, v202, v186
	v_cvt_scalef32_pk_f16_fp4 v197, v124, 1.0 op_sel:[1,1,0]
	v_pk_fma_f16 v187, v195, v202, v187
	v_cvt_scalef32_pk_f16_fp4 v194, v125, 1.0
	v_pk_fma_f16 v188, v196, v202, v188
	v_cvt_scalef32_pk_f16_fp4 v195, v125, 1.0 op_sel:[1,0,0]
	v_pk_fma_f16 v189, v197, v202, v189
	v_cvt_scalef32_pk_f16_fp4 v196, v125, 1.0 op_sel:[0,1,0]
	v_pk_fma_f16 v190, v194, v202, v190
	v_cvt_scalef32_pk_f16_fp4 v197, v125, 1.0 op_sel:[1,1,0]
	v_pk_fma_f16 v191, v195, v202, v191
	v_pk_fma_f16 v192, v196, v202, v192
	v_pk_fma_f16 v193, v197, v202, v193
	v_mul_u32_u24_sdwa v203, v145, s93 dst_sel:DWORD dst_unused:UNUSED_PAD src0_sel:WORD_1 src1_sel:DWORD
	v_cvt_scalef32_pk_f16_fp4 v194, v126, 1.0
	v_cvt_scalef32_pk_f16_fp4 v195, v126, 1.0 op_sel:[1,0,0]
	v_cvt_scalef32_pk_f16_fp4 v196, v126, 1.0 op_sel:[0,1,0]
	v_pk_fma_f16 v178, v194, v203, v178
	v_cvt_scalef32_pk_f16_fp4 v197, v126, 1.0 op_sel:[1,1,0]
	v_pk_fma_f16 v179, v195, v203, v179
	v_cvt_scalef32_pk_f16_fp4 v194, v127, 1.0
	v_pk_fma_f16 v180, v196, v203, v180
	v_cvt_scalef32_pk_f16_fp4 v195, v127, 1.0 op_sel:[1,0,0]
	v_pk_fma_f16 v181, v197, v203, v181
	v_cvt_scalef32_pk_f16_fp4 v196, v127, 1.0 op_sel:[0,1,0]
	v_pk_fma_f16 v182, v194, v203, v182
	v_cvt_scalef32_pk_f16_fp4 v197, v127, 1.0 op_sel:[1,1,0]
	v_pk_fma_f16 v183, v195, v203, v183
	v_cvt_scalef32_pk_f16_fp4 v194, v128, 1.0
	v_pk_fma_f16 v184, v196, v203, v184
	v_cvt_scalef32_pk_f16_fp4 v195, v128, 1.0 op_sel:[1,0,0]
	v_pk_fma_f16 v185, v197, v203, v185
	v_cvt_scalef32_pk_f16_fp4 v196, v128, 1.0 op_sel:[0,1,0]
	v_pk_fma_f16 v186, v194, v203, v186
	v_cvt_scalef32_pk_f16_fp4 v197, v128, 1.0 op_sel:[1,1,0]
	v_pk_fma_f16 v187, v195, v203, v187
	v_cvt_scalef32_pk_f16_fp4 v194, v129, 1.0
	v_pk_fma_f16 v188, v196, v203, v188
	v_cvt_scalef32_pk_f16_fp4 v195, v129, 1.0 op_sel:[1,0,0]
	v_pk_fma_f16 v189, v197, v203, v189
	v_cvt_scalef32_pk_f16_fp4 v196, v129, 1.0 op_sel:[0,1,0]
	v_pk_fma_f16 v190, v194, v203, v190
	v_cvt_scalef32_pk_f16_fp4 v197, v129, 1.0 op_sel:[1,1,0]
	v_pk_fma_f16 v191, v195, v203, v191
	v_pk_fma_f16 v192, v196, v203, v192
	v_pk_fma_f16 v193, v197, v203, v193
	s_nop 1
	v_permlane32_swap_b32_e32 v178, v186
	v_permlane32_swap_b32_e32 v179, v187
	v_permlane32_swap_b32_e32 v180, v188
	v_permlane32_swap_b32_e32 v181, v189
	v_permlane32_swap_b32_e32 v182, v190
	v_permlane32_swap_b32_e32 v183, v191
	v_permlane32_swap_b32_e32 v184, v192
	v_permlane32_swap_b32_e32 v185, v193
	v_pk_add_f16 v66, v178, v186
	v_pk_add_f16 v67, v179, v187
	v_pk_add_f16 v68, v180, v188
	v_pk_add_f16 v69, v181, v189
	v_pk_add_f16 v70, v182, v190
	v_pk_add_f16 v71, v183, v191
	v_pk_add_f16 v72, v184, v192
	v_pk_add_f16 v73, v185, v193
	v_cvt_f32_f16_e32 v74, v66
	v_cvt_f32_f16_sdwa v75, v66 dst_sel:DWORD dst_unused:UNUSED_PAD src0_sel:WORD_1
	v_cvt_f32_f16_e32 v76, v67
	v_cvt_f32_f16_sdwa v77, v67 dst_sel:DWORD dst_unused:UNUSED_PAD src0_sel:WORD_1
	v_cvt_f32_f16_e32 v78, v68
	v_cvt_f32_f16_sdwa v79, v68 dst_sel:DWORD dst_unused:UNUSED_PAD src0_sel:WORD_1
	v_cvt_f32_f16_e32 v80, v69
	v_cvt_f32_f16_sdwa v81, v69 dst_sel:DWORD dst_unused:UNUSED_PAD src0_sel:WORD_1
	v_cvt_f32_f16_e32 v82, v70
	v_cvt_f32_f16_sdwa v83, v70 dst_sel:DWORD dst_unused:UNUSED_PAD src0_sel:WORD_1
	v_cvt_f32_f16_e32 v84, v71
	v_cvt_f32_f16_sdwa v85, v71 dst_sel:DWORD dst_unused:UNUSED_PAD src0_sel:WORD_1
	v_cvt_f32_f16_e32 v86, v72
	v_cvt_f32_f16_sdwa v87, v72 dst_sel:DWORD dst_unused:UNUSED_PAD src0_sel:WORD_1
	v_cvt_f32_f16_e32 v88, v73
	v_cvt_f32_f16_sdwa v89, v73 dst_sel:DWORD dst_unused:UNUSED_PAD src0_sel:WORD_1
	s_nop 1
	v_permlane16_swap_b32_e32 v74, v82
	v_permlane16_swap_b32_e32 v75, v83
	v_permlane16_swap_b32_e32 v76, v84
	v_permlane16_swap_b32_e32 v77, v85
	v_permlane16_swap_b32_e32 v78, v86
	v_permlane16_swap_b32_e32 v79, v87
	v_permlane16_swap_b32_e32 v80, v88
	v_permlane16_swap_b32_e32 v81, v89
	v_add_f32_e32 v90, v74, v82
	v_add_f32_e32 v91, v75, v83
	v_add_f32_e32 v92, v76, v84
	v_add_f32_e32 v93, v77, v85
	v_add_f32_e32 v94, v78, v86
	v_add_f32_e32 v95, v79, v87
	v_add_f32_e32 v96, v80, v88
	v_add_f32_e32 v97, v81, v89
	s_nop 1
	v_add_f32_dpp v98, v90, v90 row_ror:8 row_mask:0xf bank_mask:0xf bound_ctrl:1
	v_add_f32_dpp v99, v94, v94 row_ror:8 row_mask:0xf bank_mask:0xf bound_ctrl:1
	v_add_f32_dpp v100, v91, v91 row_ror:8 row_mask:0xf bank_mask:0xf bound_ctrl:1
	v_add_f32_dpp v101, v95, v95 row_ror:8 row_mask:0xf bank_mask:0xf bound_ctrl:1
	v_add_f32_dpp v102, v92, v92 row_ror:8 row_mask:0xf bank_mask:0xf bound_ctrl:1
	v_add_f32_dpp v103, v96, v96 row_ror:8 row_mask:0xf bank_mask:0xf bound_ctrl:1
	v_add_f32_dpp v104, v93, v93 row_ror:8 row_mask:0xf bank_mask:0xf bound_ctrl:1
	v_add_f32_dpp v105, v97, v97 row_ror:8 row_mask:0xf bank_mask:0xf bound_ctrl:1
	v_cndmask_b32_e64 v106, v99, v98, s[38:39]
	v_cndmask_b32_e64 v107, v101, v100, s[38:39]
	v_cndmask_b32_e64 v108, v103, v102, s[38:39]
	v_cndmask_b32_e64 v109, v105, v104, s[38:39]
	v_fma_f32 v110, v158, v106, v154
	v_fma_f32 v111, v159, v107, v155
	v_fma_f32 v112, v160, v108, v156
	v_fma_f32 v113, v161, v109, v157
	global_store_dwordx4 v[240:241], v[110:113], off
	v_add_u32_e32 v226, 2, v226
	s_add_i32 s33, s33, 2
	s_cmp_lt_u32 s33, 8
	s_cbranch_scc1 .Le2_loop
	s_branch .LBB0_880
